# v3_fullpass
# speedup vs baseline: 1.0451x; 1.0208x over previous
.LBB1_9:
	s_waitcnt lgkmcnt(0)
	v_fma_f32 v2, s18, v1, v127
	v_fma_f32 v3, s22, v1, v128
	v_cndmask_b32_e64 v4, v3, v2, s[4:5]
	v_cndmask_b32_e64 v2, v3, v2, s[6:7]
	v_mul_f32_e32 v8, v2, v142
	v_mul_f32_e32 v2, v2, v143
	v_mul_f32_e32 v5, v4, v140
	v_mul_f32_e32 v4, v4, v141
	v_fract_f32_e32 v2, v2
	v_fract_f32_e32 v4, v4
	v_sin_f32_e32 v10, v2
	v_cos_f32_e32 v2, v2
	v_sin_f32_e32 v7, v4
	v_cos_f32_e32 v4, v4
	v_fma_f32 v1, s26, v1, v129
	v_fract_f32_e32 v5, v5
	v_sin_f32_e32 v6, v5
	v_cos_f32_e32 v5, v5
	v_cndmask_b32_e64 v1, v1, v3, s[2:3]
	v_cvt_pk_bf16_f32 v53, v10, v2
	v_mul_f32_e32 v2, v1, v144
	v_cvt_pk_bf16_f32 v51, v7, v4
	v_fract_f32_e32 v2, v2
	v_mul_f32_e32 v4, v1, v145
	v_sin_f32_e32 v3, v2
	v_cos_f32_e32 v2, v2
	v_fract_f32_e32 v4, v4
	v_cvt_pk_bf16_f32 v50, v6, v5
	v_sin_f32_e32 v5, v4
	v_cos_f32_e32 v4, v4
	v_mul_f32_e32 v6, v1, v146
	v_fract_f32_e32 v6, v6
	v_mul_f32_e32 v1, v1, v147
	v_cos_f32_e32 v7, v6
	v_cvt_pk_bf16_f32 v56, v3, v2
	v_sin_f32_e32 v2, v6
	v_fract_f32_e32 v1, v1
	v_cvt_pk_bf16_f32 v57, v5, v4
	v_cos_f32_e32 v4, v1
	v_sin_f32_e32 v1, v1
	v_cndmask_b32_e64 v3, v7, 0, s[0:1]
	v_cndmask_b32_e64 v2, v2, 1.0, s[0:1]
	v_fract_f32_e32 v8, v8
	v_cvt_pk_bf16_f32 v58, v2, v3
	v_cndmask_b32_e64 v2, v4, 0, s[0:1]
	v_cndmask_b32_e64 v1, v1, 0, s[0:1]
	v_sin_f32_e32 v9, v8
	v_cos_f32_e32 v8, v8
	v_cvt_pk_bf16_f32 v59, v1, v2
	v_fma_f32 v1, s18, v0, v127
	v_fma_f32 v2, s22, v0, v128
	v_cndmask_b32_e64 v3, v2, v1, s[4:5]
	v_cndmask_b32_e64 v1, v2, v1, s[6:7]
	v_mul_f32_e32 v7, v1, v142
	v_mul_f32_e32 v1, v1, v143
	v_mul_f32_e32 v4, v3, v140
	v_mul_f32_e32 v3, v3, v141
	v_fract_f32_e32 v1, v1
	v_cvt_pk_bf16_f32 v52, v9, v8
	v_fract_f32_e32 v3, v3
	v_sin_f32_e32 v9, v1
	v_cos_f32_e32 v1, v1
	v_sin_f32_e32 v6, v3
	v_cos_f32_e32 v3, v3
	v_fma_f32 v0, s26, v0, v129
	v_fract_f32_e32 v4, v4
	v_sin_f32_e32 v5, v4
	v_cos_f32_e32 v4, v4
	v_cndmask_b32_e64 v0, v0, v2, s[2:3]
	v_cvt_pk_bf16_f32 v63, v9, v1
	v_mul_f32_e32 v1, v0, v144
	v_cvt_pk_bf16_f32 v61, v6, v3
	v_fract_f32_e32 v1, v1
	v_mul_f32_e32 v3, v0, v145
	v_sin_f32_e32 v2, v1
	v_cos_f32_e32 v1, v1
	v_fract_f32_e32 v3, v3
	v_cvt_pk_bf16_f32 v60, v5, v4
	v_sin_f32_e32 v4, v3
	v_cos_f32_e32 v3, v3
	v_mul_f32_e32 v5, v0, v146
	v_fract_f32_e32 v5, v5
	v_mul_f32_e32 v0, v0, v147
	v_fract_f32_e32 v7, v7
	v_cos_f32_e32 v6, v5
	v_cvt_pk_bf16_f32 v72, v2, v1
	v_sin_f32_e32 v1, v5
	v_fract_f32_e32 v0, v0
	v_sin_f32_e32 v8, v7
	v_cos_f32_e32 v7, v7
	v_cvt_pk_bf16_f32 v73, v4, v3
	v_cos_f32_e32 v3, v0
	v_cndmask_b32_e64 v2, v6, 0, s[0:1]
	v_cndmask_b32_e64 v1, v1, 1.0, s[0:1]
	v_cvt_pk_bf16_f32 v62, v8, v7
	v_cvt_pk_bf16_f32 v74, v1, v2
	v_sin_f32_e32 v16, v0
	v_cndmask_b32_e64 v17, v3, 0, s[0:1]
	v_cndmask_b32_e64 v16, v16, 0, s[0:1]
	v_cvt_pk_bf16_f32 v75, v16, v17
	v_mov_b32_e32 v183, v131
	s_mov_b32 s50, 0x10000
	s_mov_b32 s52, 0
	s_waitcnt vmcnt(0) lgkmcnt(0)
	s_barrier
	ds_read_b128 v[224:227], v148 offset:0
	ds_read_b128 v[228:231], v148 offset:1024
	ds_read_b128 v[232:235], v148 offset:2048
	ds_read_b128 v[236:239], v148 offset:3072
	ds_read_b128 v[240:243], v148 offset:4096
	ds_read_b128 v[244:247], v148 offset:5120
	ds_read_b128 v[248:251], v148 offset:6144
	ds_read_b128 v[252:255], v148 offset:7168
	v_mov_b32_e32 v208, v50
	v_mov_b32_e32 v209, v51
	v_mov_b32_e32 v210, v52
	v_mov_b32_e32 v211, v53
	v_mov_b32_e32 v212, v60
	v_mov_b32_e32 v213, v61
	v_mov_b32_e32 v214, v62
	v_mov_b32_e32 v215, v63
	v_mov_b32_e32 v216, v56
	v_mov_b32_e32 v217, v57
	v_mov_b32_e32 v218, v58
	v_mov_b32_e32 v219, v59
	v_mov_b32_e32 v220, v72
	v_mov_b32_e32 v221, v73
	v_mov_b32_e32 v222, v74
	v_mov_b32_e32 v223, v75
	s_waitcnt lgkmcnt(7)
	v_mfma_f32_16x16x32_bf16 v[64:67], v[224:227], v[208:211], 0
	v_mfma_f32_16x16x32_bf16 v[56:59], v[224:227], v[212:215], 0
	ds_read_b128 v[224:227], v148 offset:8192
	s_waitcnt lgkmcnt(7)
	v_mfma_f32_16x16x32_bf16 v[68:71], v[228:231], v[208:211], 0
	v_mfma_f32_16x16x32_bf16 v[60:63], v[228:231], v[212:215], 0
	ds_read_b128 v[228:231], v148 offset:9216
	s_waitcnt lgkmcnt(7)
	v_mfma_f32_16x16x32_bf16 v[64:67], v[232:235], v[216:219], v[64:67]
	v_mfma_f32_16x16x32_bf16 v[56:59], v[232:235], v[220:223], v[56:59]
	ds_read_b128 v[232:235], v148 offset:10240
	s_waitcnt lgkmcnt(7)
	v_mfma_f32_16x16x32_bf16 v[68:71], v[236:239], v[216:219], v[68:71]
	v_mfma_f32_16x16x32_bf16 v[60:63], v[236:239], v[220:223], v[60:63]
	ds_read_b128 v[236:239], v148 offset:11264
	s_waitcnt lgkmcnt(7)
	v_mfma_f32_16x16x32_bf16 v[80:83], v[240:243], v[208:211], 0
	v_cvt_pk_bf16_f32 v0, v64, v65
	v_cvt_pk_bf16_f32 v1, v66, v67
	v_mfma_f32_16x16x32_bf16 v[84:87], v[240:243], v[212:215], 0
	v_cvt_pk_bf16_f32 v4, v56, v57
	v_cvt_pk_bf16_f32 v5, v58, v59
	ds_read_b128 v[240:243], v148 offset:12288
	s_waitcnt lgkmcnt(7)
	v_mfma_f32_16x16x32_bf16 v[76:79], v[244:247], v[208:211], 0
	v_cvt_pk_bf16_f32 v2, v68, v69
	v_cvt_pk_bf16_f32 v3, v70, v71
	s_mov_b32 m0, s28
	s_mov_b32 s51, 0x8000
	v_mfma_f32_16x16x32_bf16 v[72:75], v[244:247], v[212:215], 0
	v_cvt_pk_bf16_f32 v6, v60, v61
	v_cvt_pk_bf16_f32 v7, v62, v63
	buffer_load_dwordx4 v125, s[36:39], s51 offen lds
	ds_read_b128 v[244:247], v148 offset:13312
	s_waitcnt lgkmcnt(7)
	v_mfma_f32_16x16x32_bf16 v[80:83], v[248:251], v[216:219], v[80:83]
	v_pk_max_i16 v0, v0, 0
	v_pk_max_i16 v1, v1, 0
	v_mfma_f32_16x16x32_bf16 v[84:87], v[248:251], v[220:223], v[84:87]
	v_pk_max_i16 v2, v2, 0
	v_pk_max_i16 v3, v3, 0
	ds_read_b128 v[248:251], v148 offset:14336
	s_waitcnt lgkmcnt(7)
	v_mfma_f32_16x16x32_bf16 v[76:79], v[252:255], v[216:219], v[76:79]
	v_pk_max_i16 v4, v4, 0
	v_pk_max_i16 v5, v5, 0
	v_mfma_f32_16x16x32_bf16 v[72:75], v[252:255], v[220:223], v[72:75]
	v_pk_max_i16 v6, v6, 0
	v_pk_max_i16 v7, v7, 0
	ds_read_b128 v[252:255], v148 offset:15360
	s_waitcnt lgkmcnt(7)
	v_mfma_f32_16x16x32_bf16 v[64:67], v[224:227], v[208:211], 0
	v_cvt_pk_bf16_f32 v12, v80, v81
	v_cvt_pk_bf16_f32 v13, v82, v83
	v_mfma_f32_16x16x32_bf16 v[56:59], v[224:227], v[212:215], 0
	v_cvt_pk_bf16_f32 v8, v84, v85
	v_cvt_pk_bf16_f32 v9, v86, v87
	ds_read_b128 v[224:227], v148 offset:16384
	s_waitcnt lgkmcnt(7)
	v_mfma_f32_16x16x32_bf16 v[68:71], v[228:231], v[208:211], 0
	v_cvt_pk_bf16_f32 v14, v76, v77
	v_cvt_pk_bf16_f32 v15, v78, v79
	s_mov_b32 m0, s29
	s_mov_b32 s51, 0xa000
	v_mfma_f32_16x16x32_bf16 v[60:63], v[228:231], v[212:215], 0
	v_cvt_pk_bf16_f32 v10, v72, v73
	v_cvt_pk_bf16_f32 v11, v74, v75
	buffer_load_dwordx4 v125, s[36:39], s51 offen lds
	ds_read_b128 v[228:231], v148 offset:17408
	s_waitcnt lgkmcnt(7)
	v_mfma_f32_16x16x32_bf16 v[64:67], v[232:235], v[216:219], v[64:67]
	v_pk_max_i16 v12, v12, 0
	v_pk_max_i16 v13, v13, 0
	v_mfma_f32_16x16x32_bf16 v[56:59], v[232:235], v[220:223], v[56:59]
	v_pk_max_i16 v14, v14, 0
	v_pk_max_i16 v15, v15, 0
	ds_read_b128 v[232:235], v148 offset:18432
	s_waitcnt lgkmcnt(7)
	v_mfma_f32_16x16x32_bf16 v[68:71], v[236:239], v[216:219], v[68:71]
	v_pk_max_i16 v8, v8, 0
	v_pk_max_i16 v9, v9, 0
	v_mfma_f32_16x16x32_bf16 v[60:63], v[236:239], v[220:223], v[60:63]
	v_pk_max_i16 v10, v10, 0
	v_pk_max_i16 v11, v11, 0
	ds_read_b128 v[236:239], v148 offset:19456
	s_waitcnt lgkmcnt(7)
	v_mfma_f32_16x16x32_bf16 v[80:83], v[240:243], v[208:211], 0
	v_cvt_pk_bf16_f32 v16, v64, v65
	v_cvt_pk_bf16_f32 v17, v66, v67
	v_mfma_f32_16x16x32_bf16 v[84:87], v[240:243], v[212:215], 0
	v_cvt_pk_bf16_f32 v20, v56, v57
	v_cvt_pk_bf16_f32 v21, v58, v59
	ds_read_b128 v[240:243], v148 offset:20480
	s_waitcnt lgkmcnt(7)
	v_mfma_f32_16x16x32_bf16 v[76:79], v[244:247], v[208:211], 0
	v_cvt_pk_bf16_f32 v18, v68, v69
	v_cvt_pk_bf16_f32 v19, v70, v71
	s_mov_b32 m0, s33
	s_mov_b32 s51, 0xc000
	v_mfma_f32_16x16x32_bf16 v[72:75], v[244:247], v[212:215], 0
	v_cvt_pk_bf16_f32 v22, v60, v61
	v_cvt_pk_bf16_f32 v23, v62, v63
	buffer_load_dwordx4 v125, s[36:39], s51 offen lds
	ds_read_b128 v[244:247], v148 offset:21504
	s_waitcnt lgkmcnt(7)
	v_mfma_f32_16x16x32_bf16 v[80:83], v[248:251], v[216:219], v[80:83]
	v_pk_max_i16 v16, v16, 0
	v_pk_max_i16 v17, v17, 0
	v_mfma_f32_16x16x32_bf16 v[84:87], v[248:251], v[220:223], v[84:87]
	v_pk_max_i16 v18, v18, 0
	v_pk_max_i16 v19, v19, 0
	ds_read_b128 v[248:251], v148 offset:22528
	s_waitcnt lgkmcnt(7)
	v_mfma_f32_16x16x32_bf16 v[76:79], v[252:255], v[216:219], v[76:79]
	v_pk_max_i16 v20, v20, 0
	v_pk_max_i16 v21, v21, 0
	v_mfma_f32_16x16x32_bf16 v[72:75], v[252:255], v[220:223], v[72:75]
	v_pk_max_i16 v22, v22, 0
	v_pk_max_i16 v23, v23, 0
	ds_read_b128 v[252:255], v148 offset:23552
	s_waitcnt lgkmcnt(7)
	v_mfma_f32_16x16x32_bf16 v[64:67], v[224:227], v[208:211], 0
	v_cvt_pk_bf16_f32 v24, v80, v81
	v_cvt_pk_bf16_f32 v25, v82, v83
	v_mfma_f32_16x16x32_bf16 v[56:59], v[224:227], v[212:215], 0
	v_cvt_pk_bf16_f32 v28, v84, v85
	v_cvt_pk_bf16_f32 v29, v86, v87
	ds_read_b128 v[224:227], v148 offset:24576
	s_waitcnt lgkmcnt(7)
	v_mfma_f32_16x16x32_bf16 v[68:71], v[228:231], v[208:211], 0
	v_cvt_pk_bf16_f32 v26, v76, v77
	v_cvt_pk_bf16_f32 v27, v78, v79
	s_mov_b32 m0, s34
	s_mov_b32 s51, 0xe000
	v_mfma_f32_16x16x32_bf16 v[60:63], v[228:231], v[212:215], 0
	v_cvt_pk_bf16_f32 v30, v72, v73
	v_cvt_pk_bf16_f32 v31, v74, v75
	buffer_load_dwordx4 v125, s[36:39], s51 offen lds
	ds_read_b128 v[228:231], v148 offset:25600
	s_waitcnt lgkmcnt(7)
	v_mfma_f32_16x16x32_bf16 v[64:67], v[232:235], v[216:219], v[64:67]
	v_pk_max_i16 v24, v24, 0
	v_pk_max_i16 v25, v25, 0
	v_mfma_f32_16x16x32_bf16 v[56:59], v[232:235], v[220:223], v[56:59]
	v_pk_max_i16 v26, v26, 0
	v_pk_max_i16 v27, v27, 0
	ds_read_b128 v[232:235], v148 offset:26624
	s_waitcnt lgkmcnt(7)
	v_mfma_f32_16x16x32_bf16 v[68:71], v[236:239], v[216:219], v[68:71]
	v_pk_max_i16 v28, v28, 0
	v_pk_max_i16 v29, v29, 0
	v_mfma_f32_16x16x32_bf16 v[60:63], v[236:239], v[220:223], v[60:63]
	v_pk_max_i16 v30, v30, 0
	v_pk_max_i16 v31, v31, 0
	ds_read_b128 v[236:239], v148 offset:27648
	s_waitcnt lgkmcnt(7)
	v_mfma_f32_16x16x32_bf16 v[80:83], v[240:243], v[208:211], 0
	v_cvt_pk_bf16_f32 v32, v64, v65
	v_cvt_pk_bf16_f32 v33, v66, v67
	v_mfma_f32_16x16x32_bf16 v[84:87], v[240:243], v[212:215], 0
	v_cvt_pk_bf16_f32 v36, v56, v57
	v_cvt_pk_bf16_f32 v37, v58, v59
	ds_read_b128 v[240:243], v148 offset:28672
	s_waitcnt lgkmcnt(7)
	v_mfma_f32_16x16x32_bf16 v[76:79], v[244:247], v[208:211], 0
	v_cvt_pk_bf16_f32 v34, v68, v69
	v_cvt_pk_bf16_f32 v35, v70, v71
	v_mfma_f32_16x16x32_bf16 v[72:75], v[244:247], v[212:215], 0
	v_cvt_pk_bf16_f32 v38, v60, v61
	v_cvt_pk_bf16_f32 v39, v62, v63
	ds_read_b128 v[244:247], v148 offset:29696
	s_waitcnt lgkmcnt(7)
	v_mfma_f32_16x16x32_bf16 v[80:83], v[248:251], v[216:219], v[80:83]
	v_pk_max_i16 v32, v32, 0
	v_pk_max_i16 v33, v33, 0
	v_mfma_f32_16x16x32_bf16 v[84:87], v[248:251], v[220:223], v[84:87]
	v_pk_max_i16 v34, v34, 0
	v_pk_max_i16 v35, v35, 0
	ds_read_b128 v[248:251], v148 offset:30720
	s_waitcnt lgkmcnt(7)
	v_mfma_f32_16x16x32_bf16 v[76:79], v[252:255], v[216:219], v[76:79]
	v_pk_max_i16 v36, v36, 0
	v_pk_max_i16 v37, v37, 0
	v_mfma_f32_16x16x32_bf16 v[72:75], v[252:255], v[220:223], v[72:75]
	v_pk_max_i16 v38, v38, 0
	v_pk_max_i16 v39, v39, 0
	ds_read_b128 v[252:255], v148 offset:31744
	s_waitcnt lgkmcnt(7)
	v_mfma_f32_16x16x32_bf16 v[64:67], v[224:227], v[208:211], 0
	v_cvt_pk_bf16_f32 v40, v80, v81
	v_cvt_pk_bf16_f32 v41, v82, v83
	v_mfma_f32_16x16x32_bf16 v[56:59], v[224:227], v[212:215], 0
	v_cvt_pk_bf16_f32 v44, v84, v85
	v_cvt_pk_bf16_f32 v45, v86, v87
	s_waitcnt lgkmcnt(6)
	v_mfma_f32_16x16x32_bf16 v[68:71], v[228:231], v[208:211], 0
	v_cvt_pk_bf16_f32 v42, v76, v77
	v_cvt_pk_bf16_f32 v43, v78, v79
	v_mfma_f32_16x16x32_bf16 v[60:63], v[228:231], v[212:215], 0
	v_cvt_pk_bf16_f32 v46, v72, v73
	v_cvt_pk_bf16_f32 v47, v74, v75
	s_waitcnt lgkmcnt(5)
	v_mfma_f32_16x16x32_bf16 v[64:67], v[232:235], v[216:219], v[64:67]
	v_pk_max_i16 v40, v40, 0
	v_pk_max_i16 v41, v41, 0
	v_mfma_f32_16x16x32_bf16 v[56:59], v[232:235], v[220:223], v[56:59]
	v_pk_max_i16 v42, v42, 0
	v_pk_max_i16 v43, v43, 0
	s_waitcnt lgkmcnt(4)
	v_mfma_f32_16x16x32_bf16 v[68:71], v[236:239], v[216:219], v[68:71]
	v_pk_max_i16 v44, v44, 0
	v_pk_max_i16 v45, v45, 0
	v_mfma_f32_16x16x32_bf16 v[60:63], v[236:239], v[220:223], v[60:63]
	v_pk_max_i16 v46, v46, 0
	v_pk_max_i16 v47, v47, 0
	s_waitcnt lgkmcnt(3)
	v_mfma_f32_16x16x32_bf16 v[80:83], v[240:243], v[208:211], 0
	v_cvt_pk_bf16_f32 v48, v64, v65
	v_cvt_pk_bf16_f32 v49, v66, v67
	v_mfma_f32_16x16x32_bf16 v[84:87], v[240:243], v[212:215], 0
	v_cvt_pk_bf16_f32 v52, v56, v57
	v_cvt_pk_bf16_f32 v53, v58, v59
	s_waitcnt lgkmcnt(2)
	v_mfma_f32_16x16x32_bf16 v[76:79], v[244:247], v[208:211], 0
	v_cvt_pk_bf16_f32 v50, v68, v69
	v_cvt_pk_bf16_f32 v51, v70, v71
	v_mfma_f32_16x16x32_bf16 v[72:75], v[244:247], v[212:215], 0
	v_cvt_pk_bf16_f32 v54, v60, v61
	v_cvt_pk_bf16_f32 v55, v62, v63
	s_waitcnt lgkmcnt(1)
	v_mfma_f32_16x16x32_bf16 v[80:83], v[248:251], v[216:219], v[80:83]
	v_pk_max_i16 v48, v48, 0
	v_pk_max_i16 v49, v49, 0
	v_mfma_f32_16x16x32_bf16 v[84:87], v[248:251], v[220:223], v[84:87]
	v_pk_max_i16 v50, v50, 0
	v_pk_max_i16 v51, v51, 0
	s_waitcnt lgkmcnt(0)
	v_mfma_f32_16x16x32_bf16 v[76:79], v[252:255], v[216:219], v[76:79]
	v_pk_max_i16 v52, v52, 0
	v_pk_max_i16 v53, v53, 0
	v_mfma_f32_16x16x32_bf16 v[72:75], v[252:255], v[220:223], v[72:75]
	v_pk_max_i16 v54, v54, 0
	v_pk_max_i16 v55, v55, 0
	s_waitcnt vmcnt(0) lgkmcnt(0)
	s_barrier
	ds_read_b128 v[224:227], v121 offset:40960
	ds_read_b128 v[228:231], v121 offset:41984
	ds_read_b128 v[64:67], v183 offset:0
	ds_read_b128 v[56:59], v183 offset:0
	ds_read_b128 v[68:71], v183 offset:64
	ds_read_b128 v[60:63], v183 offset:64
	ds_read_b128 v[232:235], v121 offset:43008
	ds_read_b128 v[236:239], v121 offset:44032
	ds_read_b128 v[240:243], v121 offset:45056
	ds_read_b128 v[244:247], v121 offset:46080
	ds_read_b128 v[248:251], v121 offset:47104
	ds_read_b128 v[252:255], v121 offset:48128
	s_setprio 3
	s_waitcnt lgkmcnt(6)
	v_mfma_f32_16x16x32_bf16 v[64:67], v[224:227], v[0:3], v[64:67]
	v_cvt_pk_bf16_f32 v112, v80, v81
	v_mfma_f32_16x16x32_bf16 v[68:71], v[228:231], v[0:3], v[68:71]
	v_cvt_pk_bf16_f32 v113, v82, v83
	v_mfma_f32_16x16x32_bf16 v[60:63], v[228:231], v[4:7], v[60:63]
	v_cvt_pk_bf16_f32 v114, v76, v77
	v_mfma_f32_16x16x32_bf16 v[56:59], v[224:227], v[4:7], v[56:59]
	v_cvt_pk_bf16_f32 v115, v78, v79
	ds_read_b128 v[224:227], v121 offset:49152
	ds_read_b128 v[228:231], v121 offset:50176
	s_waitcnt lgkmcnt(6)
	v_mfma_f32_16x16x32_bf16 v[64:67], v[232:235], v[12:15], v[64:67]
	v_cvt_pk_bf16_f32 v116, v84, v85
	v_mfma_f32_16x16x32_bf16 v[68:71], v[236:239], v[12:15], v[68:71]
	s_mov_b32 m0, s35
	s_add_i32 s51, s50, 0x0
	v_cvt_pk_bf16_f32 v117, v86, v87
	v_mfma_f32_16x16x32_bf16 v[60:63], v[236:239], v[8:11], v[60:63]
	buffer_load_dwordx4 v125, s[36:39], s51 offen lds
	v_cvt_pk_bf16_f32 v118, v72, v73
	v_mfma_f32_16x16x32_bf16 v[56:59], v[232:235], v[8:11], v[56:59]
	v_cvt_pk_bf16_f32 v119, v74, v75
	ds_read_b128 v[232:235], v121 offset:51200
	ds_read_b128 v[236:239], v121 offset:52224
	s_waitcnt lgkmcnt(6)
	v_mfma_f32_16x16x32_bf16 v[64:67], v[240:243], v[16:19], v[64:67]
	v_pk_max_i16 v112, v112, 0
	v_mfma_f32_16x16x32_bf16 v[68:71], v[244:247], v[16:19], v[68:71]
	s_mov_b32 m0, s42
	s_add_i32 s51, s50, 0x2000
	v_pk_max_i16 v113, v113, 0
	v_mfma_f32_16x16x32_bf16 v[60:63], v[244:247], v[20:23], v[60:63]
	buffer_load_dwordx4 v125, s[36:39], s51 offen lds
	v_pk_max_i16 v114, v114, 0
	v_mfma_f32_16x16x32_bf16 v[56:59], v[240:243], v[20:23], v[56:59]
	v_pk_max_i16 v115, v115, 0
	ds_read_b128 v[240:243], v121 offset:53248
	ds_read_b128 v[244:247], v121 offset:54272
	s_waitcnt lgkmcnt(6)
	v_mfma_f32_16x16x32_bf16 v[64:67], v[248:251], v[24:27], v[64:67]
	v_pk_max_i16 v116, v116, 0
	v_mfma_f32_16x16x32_bf16 v[68:71], v[252:255], v[24:27], v[68:71]
	s_mov_b32 m0, s41
	s_add_i32 s51, s50, 0x4000
	v_pk_max_i16 v117, v117, 0
	v_mfma_f32_16x16x32_bf16 v[60:63], v[252:255], v[28:31], v[60:63]
	buffer_load_dwordx4 v125, s[36:39], s51 offen lds
	v_pk_max_i16 v118, v118, 0
	v_mfma_f32_16x16x32_bf16 v[56:59], v[248:251], v[28:31], v[56:59]
	v_pk_max_i16 v119, v119, 0
	ds_read_b128 v[248:251], v121 offset:55296
	ds_read_b128 v[252:255], v121 offset:56320
	s_setprio 2
	s_waitcnt lgkmcnt(6)
	v_mfma_f32_16x16x32_bf16 v[64:67], v[224:227], v[32:35], v[64:67]
	ds_read_b128 v[80:83], v183 offset:128
	ds_read_b128 v[84:87], v183 offset:128
	ds_read_b128 v[76:79], v183 offset:192
	ds_read_b128 v[72:75], v183 offset:192
	v_mfma_f32_16x16x32_bf16 v[68:71], v[228:231], v[32:35], v[68:71]
	s_mov_b32 m0, s40
	s_add_i32 s51, s50, 0x6000
	v_mfma_f32_16x16x32_bf16 v[60:63], v[228:231], v[36:39], v[60:63]
	buffer_load_dwordx4 v125, s[36:39], s51 offen lds
	v_mfma_f32_16x16x32_bf16 v[56:59], v[224:227], v[36:39], v[56:59]
	ds_read_b128 v[224:227], v121 offset:57344
	ds_read_b128 v[228:231], v121 offset:58368
	s_waitcnt lgkmcnt(10)
	v_mfma_f32_16x16x32_bf16 v[64:67], v[232:235], v[40:43], v[64:67]
	v_mfma_f32_16x16x32_bf16 v[68:71], v[236:239], v[40:43], v[68:71]
	v_mfma_f32_16x16x32_bf16 v[60:63], v[236:239], v[44:47], v[60:63]
	v_mfma_f32_16x16x32_bf16 v[56:59], v[232:235], v[44:47], v[56:59]
	ds_read_b128 v[232:235], v121 offset:59392
	ds_read_b128 v[236:239], v121 offset:60416
	s_waitcnt lgkmcnt(10)
	v_mfma_f32_16x16x32_bf16 v[64:67], v[240:243], v[48:51], v[64:67]
	v_mfma_f32_16x16x32_bf16 v[68:71], v[244:247], v[48:51], v[68:71]
	v_mfma_f32_16x16x32_bf16 v[60:63], v[244:247], v[52:55], v[60:63]
	v_mfma_f32_16x16x32_bf16 v[56:59], v[240:243], v[52:55], v[56:59]
	ds_read_b128 v[240:243], v121 offset:61440
	ds_read_b128 v[244:247], v121 offset:62464
	s_waitcnt lgkmcnt(10)
	v_mfma_f32_16x16x32_bf16 v[64:67], v[248:251], v[112:115], v[64:67]
	v_mfma_f32_16x16x32_bf16 v[68:71], v[252:255], v[112:115], v[68:71]
	v_mfma_f32_16x16x32_bf16 v[60:63], v[252:255], v[116:119], v[60:63]
	v_mfma_f32_16x16x32_bf16 v[56:59], v[248:251], v[116:119], v[56:59]
	ds_read_b128 v[248:251], v121 offset:63488
	ds_read_b128 v[252:255], v121 offset:64512
	s_setprio 1
	s_waitcnt lgkmcnt(6)
	v_mfma_f32_16x16x32_bf16 v[80:83], v[224:227], v[0:3], v[80:83]
	v_mfma_f32_16x16x32_bf16 v[76:79], v[228:231], v[0:3], v[76:79]
	v_mfma_f32_16x16x32_bf16 v[72:75], v[228:231], v[4:7], v[72:75]
	v_mfma_f32_16x16x32_bf16 v[84:87], v[224:227], v[4:7], v[84:87]
	ds_read_b128 v[224:227], v126 offset:57344
	ds_read_b128 v[228:231], v126 offset:58368
	s_waitcnt lgkmcnt(6)
	v_mfma_f32_16x16x32_bf16 v[80:83], v[232:235], v[12:15], v[80:83]
	v_cvt_pk_bf16_f32 v88, v64, v65
	v_mfma_f32_16x16x32_bf16 v[76:79], v[236:239], v[12:15], v[76:79]
	v_cvt_pk_bf16_f32 v89, v66, v67
	v_mfma_f32_16x16x32_bf16 v[72:75], v[236:239], v[8:11], v[72:75]
	v_cvt_pk_bf16_f32 v90, v68, v69
	v_mfma_f32_16x16x32_bf16 v[84:87], v[232:235], v[8:11], v[84:87]
	v_cvt_pk_bf16_f32 v91, v70, v71
	ds_read_b128 v[232:235], v126 offset:59392
	ds_read_b128 v[236:239], v126 offset:60416
	s_waitcnt lgkmcnt(6)
	v_mfma_f32_16x16x32_bf16 v[80:83], v[240:243], v[16:19], v[80:83]
	v_cvt_pk_bf16_f32 v92, v56, v57
	v_mfma_f32_16x16x32_bf16 v[76:79], v[244:247], v[16:19], v[76:79]
	v_cvt_pk_bf16_f32 v93, v58, v59
	v_mfma_f32_16x16x32_bf16 v[72:75], v[244:247], v[20:23], v[72:75]
	v_cvt_pk_bf16_f32 v94, v60, v61
	v_mfma_f32_16x16x32_bf16 v[84:87], v[240:243], v[20:23], v[84:87]
	v_cvt_pk_bf16_f32 v95, v62, v63
	ds_read_b128 v[240:243], v126 offset:61440
	ds_read_b128 v[244:247], v126 offset:62464
	s_waitcnt lgkmcnt(6)
	v_mfma_f32_16x16x32_bf16 v[80:83], v[248:251], v[24:27], v[80:83]
	v_pk_max_i16 v88, v88, 0
	v_mfma_f32_16x16x32_bf16 v[76:79], v[252:255], v[24:27], v[76:79]
	v_pk_max_i16 v89, v89, 0
	v_mfma_f32_16x16x32_bf16 v[72:75], v[252:255], v[28:31], v[72:75]
	v_pk_max_i16 v90, v90, 0
	v_mfma_f32_16x16x32_bf16 v[84:87], v[248:251], v[28:31], v[84:87]
	v_pk_max_i16 v91, v91, 0
	ds_read_b128 v[248:251], v126 offset:63488
	ds_read_b128 v[252:255], v126 offset:64512
	s_setprio 0
	s_waitcnt lgkmcnt(6)
	v_mfma_f32_16x16x32_bf16 v[80:83], v[224:227], v[32:35], v[80:83]
	v_pk_max_i16 v92, v92, 0
	v_mfma_f32_16x16x32_bf16 v[76:79], v[228:231], v[32:35], v[76:79]
	v_pk_max_i16 v93, v93, 0
	v_mfma_f32_16x16x32_bf16 v[72:75], v[228:231], v[36:39], v[72:75]
	v_pk_max_i16 v94, v94, 0
	v_mfma_f32_16x16x32_bf16 v[84:87], v[224:227], v[36:39], v[84:87]
	v_pk_max_i16 v95, v95, 0
	s_waitcnt lgkmcnt(4)
	v_mfma_f32_16x16x32_bf16 v[80:83], v[232:235], v[40:43], v[80:83]
	v_mfma_f32_16x16x32_bf16 v[76:79], v[236:239], v[40:43], v[76:79]
	v_mfma_f32_16x16x32_bf16 v[72:75], v[236:239], v[44:47], v[72:75]
	v_mfma_f32_16x16x32_bf16 v[84:87], v[232:235], v[44:47], v[84:87]
	s_branch .Lnerf_hid_b1
.Lnerf_hid_b0:
	s_waitcnt vmcnt(0) lgkmcnt(0)
	s_barrier
	ds_read_b128 v[224:227], v121 offset:40960
	ds_read_b128 v[228:231], v121 offset:41984
	ds_read_b128 v[64:67], v183 offset:0
	ds_read_b128 v[56:59], v183 offset:0
	ds_read_b128 v[68:71], v183 offset:64
	ds_read_b128 v[60:63], v183 offset:64
	v_mfma_f32_16x16x32_bf16 v[80:83], v[240:243], v[208:211], v[80:83]
	ds_read_b128 v[232:235], v121 offset:43008
	v_mfma_f32_16x16x32_bf16 v[76:79], v[244:247], v[208:211], v[76:79]
	ds_read_b128 v[236:239], v121 offset:44032
	v_mfma_f32_16x16x32_bf16 v[72:75], v[244:247], v[212:215], v[72:75]
	v_mfma_f32_16x16x32_bf16 v[84:87], v[240:243], v[212:215], v[84:87]
	ds_read_b128 v[240:243], v121 offset:45056
	ds_read_b128 v[244:247], v121 offset:46080
	v_mfma_f32_16x16x32_bf16 v[80:83], v[248:251], v[216:219], v[80:83]
	v_mfma_f32_16x16x32_bf16 v[76:79], v[252:255], v[216:219], v[76:79]
	v_mfma_f32_16x16x32_bf16 v[72:75], v[252:255], v[220:223], v[72:75]
	v_mfma_f32_16x16x32_bf16 v[84:87], v[248:251], v[220:223], v[84:87]
	ds_read_b128 v[248:251], v121 offset:47104
	ds_read_b128 v[252:255], v121 offset:48128
	s_setprio 3
	s_waitcnt lgkmcnt(6)
	v_mfma_f32_16x16x32_bf16 v[64:67], v[224:227], v[0:3], v[64:67]
	v_mfma_f32_16x16x32_bf16 v[68:71], v[228:231], v[0:3], v[68:71]
	v_mfma_f32_16x16x32_bf16 v[60:63], v[228:231], v[4:7], v[60:63]
	v_mfma_f32_16x16x32_bf16 v[56:59], v[224:227], v[4:7], v[56:59]
	ds_read_b128 v[224:227], v121 offset:49152
	ds_read_b128 v[228:231], v121 offset:50176
	s_waitcnt lgkmcnt(6)
	v_mfma_f32_16x16x32_bf16 v[64:67], v[232:235], v[12:15], v[64:67]
	v_cvt_pk_bf16_f32 v112, v80, v81
	v_mfma_f32_16x16x32_bf16 v[68:71], v[236:239], v[12:15], v[68:71]
	s_mov_b32 m0, s35
	s_add_i32 s51, s50, 0x0
	v_cvt_pk_bf16_f32 v113, v82, v83
	v_mfma_f32_16x16x32_bf16 v[60:63], v[236:239], v[8:11], v[60:63]
	buffer_load_dwordx4 v125, s[36:39], s51 offen lds
	v_cvt_pk_bf16_f32 v114, v76, v77
	v_mfma_f32_16x16x32_bf16 v[56:59], v[232:235], v[8:11], v[56:59]
	v_cvt_pk_bf16_f32 v115, v78, v79
	ds_read_b128 v[232:235], v121 offset:51200
	ds_read_b128 v[236:239], v121 offset:52224
	s_waitcnt lgkmcnt(6)
	v_mfma_f32_16x16x32_bf16 v[64:67], v[240:243], v[16:19], v[64:67]
	v_cvt_pk_bf16_f32 v116, v84, v85
	v_mfma_f32_16x16x32_bf16 v[68:71], v[244:247], v[16:19], v[68:71]
	s_mov_b32 m0, s42
	s_add_i32 s51, s50, 0x2000
	v_cvt_pk_bf16_f32 v117, v86, v87
	v_mfma_f32_16x16x32_bf16 v[60:63], v[244:247], v[20:23], v[60:63]
	buffer_load_dwordx4 v125, s[36:39], s51 offen lds
	v_cvt_pk_bf16_f32 v118, v72, v73
	v_mfma_f32_16x16x32_bf16 v[56:59], v[240:243], v[20:23], v[56:59]
	v_cvt_pk_bf16_f32 v119, v74, v75
	ds_read_b128 v[240:243], v121 offset:53248
	ds_read_b128 v[244:247], v121 offset:54272
	s_waitcnt lgkmcnt(6)
	v_mfma_f32_16x16x32_bf16 v[64:67], v[248:251], v[24:27], v[64:67]
	v_pk_max_i16 v112, v112, 0
	v_mfma_f32_16x16x32_bf16 v[68:71], v[252:255], v[24:27], v[68:71]
	s_mov_b32 m0, s41
	s_add_i32 s51, s50, 0x4000
	v_pk_max_i16 v113, v113, 0
	v_mfma_f32_16x16x32_bf16 v[60:63], v[252:255], v[28:31], v[60:63]
	buffer_load_dwordx4 v125, s[36:39], s51 offen lds
	v_pk_max_i16 v114, v114, 0
	v_mfma_f32_16x16x32_bf16 v[56:59], v[248:251], v[28:31], v[56:59]
	v_pk_max_i16 v115, v115, 0
	ds_read_b128 v[248:251], v121 offset:55296
	ds_read_b128 v[252:255], v121 offset:56320
	s_setprio 2
	s_waitcnt lgkmcnt(6)
	v_mfma_f32_16x16x32_bf16 v[64:67], v[224:227], v[32:35], v[64:67]
	v_pk_max_i16 v116, v116, 0
	v_mfma_f32_16x16x32_bf16 v[68:71], v[228:231], v[32:35], v[68:71]
	s_mov_b32 m0, s40
	s_add_i32 s51, s50, 0x6000
	v_pk_max_i16 v117, v117, 0
	v_mfma_f32_16x16x32_bf16 v[60:63], v[228:231], v[36:39], v[60:63]
	buffer_load_dwordx4 v125, s[36:39], s51 offen lds
	v_pk_max_i16 v118, v118, 0
	v_mfma_f32_16x16x32_bf16 v[56:59], v[224:227], v[36:39], v[56:59]
	v_pk_max_i16 v119, v119, 0
	ds_read_b128 v[224:227], v121 offset:57344
	ds_read_b128 v[228:231], v121 offset:58368
	s_waitcnt lgkmcnt(6)
	v_mfma_f32_16x16x32_bf16 v[64:67], v[232:235], v[40:43], v[64:67]
	ds_read_b128 v[80:83], v183 offset:128
	ds_read_b128 v[84:87], v183 offset:128
	ds_read_b128 v[76:79], v183 offset:192
	ds_read_b128 v[72:75], v183 offset:192
	v_mfma_f32_16x16x32_bf16 v[68:71], v[236:239], v[40:43], v[68:71]
	v_mfma_f32_16x16x32_bf16 v[60:63], v[236:239], v[44:47], v[60:63]
	v_mfma_f32_16x16x32_bf16 v[56:59], v[232:235], v[44:47], v[56:59]
	ds_read_b128 v[232:235], v121 offset:59392
	ds_read_b128 v[236:239], v121 offset:60416
	s_waitcnt lgkmcnt(10)
	v_mfma_f32_16x16x32_bf16 v[64:67], v[240:243], v[48:51], v[64:67]
	v_mfma_f32_16x16x32_bf16 v[68:71], v[244:247], v[48:51], v[68:71]
	v_mfma_f32_16x16x32_bf16 v[60:63], v[244:247], v[52:55], v[60:63]
	v_mfma_f32_16x16x32_bf16 v[56:59], v[240:243], v[52:55], v[56:59]
	ds_read_b128 v[240:243], v121 offset:61440
	ds_read_b128 v[244:247], v121 offset:62464
	s_waitcnt lgkmcnt(10)
	v_mfma_f32_16x16x32_bf16 v[64:67], v[248:251], v[112:115], v[64:67]
	v_mfma_f32_16x16x32_bf16 v[68:71], v[252:255], v[112:115], v[68:71]
	v_mfma_f32_16x16x32_bf16 v[60:63], v[252:255], v[116:119], v[60:63]
	v_mfma_f32_16x16x32_bf16 v[56:59], v[248:251], v[116:119], v[56:59]
	ds_read_b128 v[248:251], v121 offset:63488
	ds_read_b128 v[252:255], v121 offset:64512
	s_setprio 1
	s_waitcnt lgkmcnt(6)
	v_mfma_f32_16x16x32_bf16 v[80:83], v[224:227], v[0:3], v[80:83]
	v_mfma_f32_16x16x32_bf16 v[76:79], v[228:231], v[0:3], v[76:79]
	v_mfma_f32_16x16x32_bf16 v[72:75], v[228:231], v[4:7], v[72:75]
	v_mfma_f32_16x16x32_bf16 v[84:87], v[224:227], v[4:7], v[84:87]
	ds_read_b128 v[224:227], v126 offset:57344
	ds_read_b128 v[228:231], v126 offset:58368
	s_waitcnt lgkmcnt(6)
	v_mfma_f32_16x16x32_bf16 v[80:83], v[232:235], v[12:15], v[80:83]
	v_cvt_pk_bf16_f32 v88, v64, v65
	v_mfma_f32_16x16x32_bf16 v[76:79], v[236:239], v[12:15], v[76:79]
	v_cvt_pk_bf16_f32 v89, v66, v67
	v_mfma_f32_16x16x32_bf16 v[72:75], v[236:239], v[8:11], v[72:75]
	v_cvt_pk_bf16_f32 v90, v68, v69
	v_mfma_f32_16x16x32_bf16 v[84:87], v[232:235], v[8:11], v[84:87]
	v_cvt_pk_bf16_f32 v91, v70, v71
	ds_read_b128 v[232:235], v126 offset:59392
	ds_read_b128 v[236:239], v126 offset:60416
	s_waitcnt lgkmcnt(6)
	v_mfma_f32_16x16x32_bf16 v[80:83], v[240:243], v[16:19], v[80:83]
	v_cvt_pk_bf16_f32 v92, v56, v57
	v_mfma_f32_16x16x32_bf16 v[76:79], v[244:247], v[16:19], v[76:79]
	v_cvt_pk_bf16_f32 v93, v58, v59
	v_mfma_f32_16x16x32_bf16 v[72:75], v[244:247], v[20:23], v[72:75]
	v_cvt_pk_bf16_f32 v94, v60, v61
	v_mfma_f32_16x16x32_bf16 v[84:87], v[240:243], v[20:23], v[84:87]
	v_cvt_pk_bf16_f32 v95, v62, v63
	ds_read_b128 v[240:243], v126 offset:61440
	ds_read_b128 v[244:247], v126 offset:62464
	s_waitcnt lgkmcnt(6)
	v_mfma_f32_16x16x32_bf16 v[80:83], v[248:251], v[24:27], v[80:83]
	v_pk_max_i16 v88, v88, 0
	v_mfma_f32_16x16x32_bf16 v[76:79], v[252:255], v[24:27], v[76:79]
	v_pk_max_i16 v89, v89, 0
	v_mfma_f32_16x16x32_bf16 v[72:75], v[252:255], v[28:31], v[72:75]
	v_pk_max_i16 v90, v90, 0
	v_mfma_f32_16x16x32_bf16 v[84:87], v[248:251], v[28:31], v[84:87]
	v_pk_max_i16 v91, v91, 0
	ds_read_b128 v[248:251], v126 offset:63488
	ds_read_b128 v[252:255], v126 offset:64512
	s_setprio 0
	s_waitcnt lgkmcnt(6)
	v_mfma_f32_16x16x32_bf16 v[80:83], v[224:227], v[32:35], v[80:83]
	v_pk_max_i16 v92, v92, 0
	v_mfma_f32_16x16x32_bf16 v[76:79], v[228:231], v[32:35], v[76:79]
	v_pk_max_i16 v93, v93, 0
	v_mfma_f32_16x16x32_bf16 v[72:75], v[228:231], v[36:39], v[72:75]
	v_pk_max_i16 v94, v94, 0
	v_mfma_f32_16x16x32_bf16 v[84:87], v[224:227], v[36:39], v[84:87]
	v_pk_max_i16 v95, v95, 0
	s_waitcnt lgkmcnt(4)
	v_mfma_f32_16x16x32_bf16 v[80:83], v[232:235], v[40:43], v[80:83]
	v_mfma_f32_16x16x32_bf16 v[76:79], v[236:239], v[40:43], v[76:79]
	v_mfma_f32_16x16x32_bf16 v[72:75], v[236:239], v[44:47], v[72:75]
	v_mfma_f32_16x16x32_bf16 v[84:87], v[232:235], v[44:47], v[84:87]
.Lnerf_hid_b1:
	s_waitcnt vmcnt(0) lgkmcnt(0)
	s_barrier
	ds_read_b128 v[224:227], v121 offset:8192
	ds_read_b128 v[228:231], v121 offset:9216
	ds_read_b128 v[64:67], v183 offset:256
	ds_read_b128 v[56:59], v183 offset:256
	ds_read_b128 v[68:71], v183 offset:320
	ds_read_b128 v[60:63], v183 offset:320
	v_mfma_f32_16x16x32_bf16 v[80:83], v[240:243], v[48:51], v[80:83]
	ds_read_b128 v[232:235], v121 offset:10240
	v_mfma_f32_16x16x32_bf16 v[76:79], v[244:247], v[48:51], v[76:79]
	ds_read_b128 v[236:239], v121 offset:11264
	v_mfma_f32_16x16x32_bf16 v[72:75], v[244:247], v[52:55], v[72:75]
	v_mfma_f32_16x16x32_bf16 v[84:87], v[240:243], v[52:55], v[84:87]
	ds_read_b128 v[240:243], v121 offset:12288
	ds_read_b128 v[244:247], v121 offset:13312
	v_mfma_f32_16x16x32_bf16 v[80:83], v[248:251], v[112:115], v[80:83]
	v_mfma_f32_16x16x32_bf16 v[76:79], v[252:255], v[112:115], v[76:79]
	v_mfma_f32_16x16x32_bf16 v[72:75], v[252:255], v[116:119], v[72:75]
	v_mfma_f32_16x16x32_bf16 v[84:87], v[248:251], v[116:119], v[84:87]
	ds_read_b128 v[248:251], v121 offset:14336
	ds_read_b128 v[252:255], v121 offset:15360
	s_setprio 3
	s_waitcnt lgkmcnt(6)
	v_mfma_f32_16x16x32_bf16 v[64:67], v[224:227], v[0:3], v[64:67]
	v_mfma_f32_16x16x32_bf16 v[68:71], v[228:231], v[0:3], v[68:71]
	v_mfma_f32_16x16x32_bf16 v[60:63], v[228:231], v[4:7], v[60:63]
	v_mfma_f32_16x16x32_bf16 v[56:59], v[224:227], v[4:7], v[56:59]
	ds_read_b128 v[224:227], v121 offset:16384
	ds_read_b128 v[228:231], v121 offset:17408
	s_waitcnt lgkmcnt(6)
	v_mfma_f32_16x16x32_bf16 v[64:67], v[232:235], v[12:15], v[64:67]
	v_cvt_pk_bf16_f32 v96, v80, v81
	v_mfma_f32_16x16x32_bf16 v[68:71], v[236:239], v[12:15], v[68:71]
	s_mov_b32 m0, s28
	s_add_i32 s51, s50, 0x8000
	v_cvt_pk_bf16_f32 v97, v82, v83
	v_mfma_f32_16x16x32_bf16 v[60:63], v[236:239], v[8:11], v[60:63]
	buffer_load_dwordx4 v125, s[36:39], s51 offen lds
	v_cvt_pk_bf16_f32 v98, v76, v77
	v_mfma_f32_16x16x32_bf16 v[56:59], v[232:235], v[8:11], v[56:59]
	v_cvt_pk_bf16_f32 v99, v78, v79
	ds_read_b128 v[232:235], v121 offset:18432
	ds_read_b128 v[236:239], v121 offset:19456
	s_waitcnt lgkmcnt(6)
	v_mfma_f32_16x16x32_bf16 v[64:67], v[240:243], v[16:19], v[64:67]
	v_cvt_pk_bf16_f32 v100, v84, v85
	v_mfma_f32_16x16x32_bf16 v[68:71], v[244:247], v[16:19], v[68:71]
	s_mov_b32 m0, s29
	s_add_i32 s51, s50, 0xa000
	v_cvt_pk_bf16_f32 v101, v86, v87
	v_mfma_f32_16x16x32_bf16 v[60:63], v[244:247], v[20:23], v[60:63]
	buffer_load_dwordx4 v125, s[36:39], s51 offen lds
	v_cvt_pk_bf16_f32 v102, v72, v73
	v_mfma_f32_16x16x32_bf16 v[56:59], v[240:243], v[20:23], v[56:59]
	v_cvt_pk_bf16_f32 v103, v74, v75
	ds_read_b128 v[240:243], v121 offset:20480
	ds_read_b128 v[244:247], v121 offset:21504
	s_waitcnt lgkmcnt(6)
	v_mfma_f32_16x16x32_bf16 v[64:67], v[248:251], v[24:27], v[64:67]
	v_pk_max_i16 v96, v96, 0
	v_mfma_f32_16x16x32_bf16 v[68:71], v[252:255], v[24:27], v[68:71]
	s_mov_b32 m0, s33
	s_add_i32 s51, s50, 0xc000
	v_pk_max_i16 v97, v97, 0
	v_mfma_f32_16x16x32_bf16 v[60:63], v[252:255], v[28:31], v[60:63]
	buffer_load_dwordx4 v125, s[36:39], s51 offen lds
	v_pk_max_i16 v98, v98, 0
	v_mfma_f32_16x16x32_bf16 v[56:59], v[248:251], v[28:31], v[56:59]
	v_pk_max_i16 v99, v99, 0
	ds_read_b128 v[248:251], v121 offset:22528
	ds_read_b128 v[252:255], v121 offset:23552
	s_setprio 2
	s_waitcnt lgkmcnt(6)
	v_mfma_f32_16x16x32_bf16 v[64:67], v[224:227], v[32:35], v[64:67]
	v_pk_max_i16 v100, v100, 0
	v_mfma_f32_16x16x32_bf16 v[68:71], v[228:231], v[32:35], v[68:71]
	s_mov_b32 m0, s34
	s_add_i32 s51, s50, 0xe000
	v_pk_max_i16 v101, v101, 0
	v_mfma_f32_16x16x32_bf16 v[60:63], v[228:231], v[36:39], v[60:63]
	buffer_load_dwordx4 v125, s[36:39], s51 offen lds
	v_pk_max_i16 v102, v102, 0
	v_mfma_f32_16x16x32_bf16 v[56:59], v[224:227], v[36:39], v[56:59]
	v_pk_max_i16 v103, v103, 0
	ds_read_b128 v[224:227], v121 offset:24576
	ds_read_b128 v[228:231], v121 offset:25600
	s_waitcnt lgkmcnt(6)
	v_mfma_f32_16x16x32_bf16 v[64:67], v[232:235], v[40:43], v[64:67]
	ds_read_b128 v[80:83], v183 offset:384
	ds_read_b128 v[84:87], v183 offset:384
	ds_read_b128 v[76:79], v183 offset:448
	ds_read_b128 v[72:75], v183 offset:448
	v_mfma_f32_16x16x32_bf16 v[68:71], v[236:239], v[40:43], v[68:71]
	v_mfma_f32_16x16x32_bf16 v[60:63], v[236:239], v[44:47], v[60:63]
	v_mfma_f32_16x16x32_bf16 v[56:59], v[232:235], v[44:47], v[56:59]
	ds_read_b128 v[232:235], v121 offset:26624
	ds_read_b128 v[236:239], v121 offset:27648
	s_waitcnt lgkmcnt(10)
	v_mfma_f32_16x16x32_bf16 v[64:67], v[240:243], v[48:51], v[64:67]
	v_mfma_f32_16x16x32_bf16 v[68:71], v[244:247], v[48:51], v[68:71]
	v_mfma_f32_16x16x32_bf16 v[60:63], v[244:247], v[52:55], v[60:63]
	v_mfma_f32_16x16x32_bf16 v[56:59], v[240:243], v[52:55], v[56:59]
	ds_read_b128 v[240:243], v121 offset:28672
	ds_read_b128 v[244:247], v121 offset:29696
	s_waitcnt lgkmcnt(10)
	v_mfma_f32_16x16x32_bf16 v[64:67], v[248:251], v[112:115], v[64:67]
	v_mfma_f32_16x16x32_bf16 v[68:71], v[252:255], v[112:115], v[68:71]
	v_mfma_f32_16x16x32_bf16 v[60:63], v[252:255], v[116:119], v[60:63]
	v_mfma_f32_16x16x32_bf16 v[56:59], v[248:251], v[116:119], v[56:59]
	ds_read_b128 v[248:251], v121 offset:30720
	ds_read_b128 v[252:255], v121 offset:31744
	s_setprio 1
	s_waitcnt lgkmcnt(6)
	v_mfma_f32_16x16x32_bf16 v[80:83], v[224:227], v[0:3], v[80:83]
	v_mfma_f32_16x16x32_bf16 v[76:79], v[228:231], v[0:3], v[76:79]
	v_mfma_f32_16x16x32_bf16 v[72:75], v[228:231], v[4:7], v[72:75]
	v_mfma_f32_16x16x32_bf16 v[84:87], v[224:227], v[4:7], v[84:87]
	ds_read_b128 v[224:227], v121 offset:32768
	ds_read_b128 v[228:231], v121 offset:33792
	s_waitcnt lgkmcnt(6)
	v_mfma_f32_16x16x32_bf16 v[80:83], v[232:235], v[12:15], v[80:83]
	v_cvt_pk_bf16_f32 v104, v64, v65
	v_mfma_f32_16x16x32_bf16 v[76:79], v[236:239], v[12:15], v[76:79]
	v_cvt_pk_bf16_f32 v105, v66, v67
	v_mfma_f32_16x16x32_bf16 v[72:75], v[236:239], v[8:11], v[72:75]
	v_cvt_pk_bf16_f32 v106, v68, v69
	v_mfma_f32_16x16x32_bf16 v[84:87], v[232:235], v[8:11], v[84:87]
	v_cvt_pk_bf16_f32 v107, v70, v71
	ds_read_b128 v[232:235], v121 offset:34816
	ds_read_b128 v[236:239], v121 offset:35840
	s_waitcnt lgkmcnt(6)
	v_mfma_f32_16x16x32_bf16 v[80:83], v[240:243], v[16:19], v[80:83]
	v_cvt_pk_bf16_f32 v108, v56, v57
	v_mfma_f32_16x16x32_bf16 v[76:79], v[244:247], v[16:19], v[76:79]
	v_cvt_pk_bf16_f32 v109, v58, v59
	v_mfma_f32_16x16x32_bf16 v[72:75], v[244:247], v[20:23], v[72:75]
	v_cvt_pk_bf16_f32 v110, v60, v61
	v_mfma_f32_16x16x32_bf16 v[84:87], v[240:243], v[20:23], v[84:87]
	v_cvt_pk_bf16_f32 v111, v62, v63
	ds_read_b128 v[240:243], v121 offset:36864
	ds_read_b128 v[244:247], v121 offset:37888
	s_waitcnt lgkmcnt(6)
	v_mfma_f32_16x16x32_bf16 v[80:83], v[248:251], v[24:27], v[80:83]
	v_pk_max_i16 v104, v104, 0
	v_mfma_f32_16x16x32_bf16 v[76:79], v[252:255], v[24:27], v[76:79]
	v_pk_max_i16 v105, v105, 0
	v_mfma_f32_16x16x32_bf16 v[72:75], v[252:255], v[28:31], v[72:75]
	v_pk_max_i16 v106, v106, 0
	v_mfma_f32_16x16x32_bf16 v[84:87], v[248:251], v[28:31], v[84:87]
	v_pk_max_i16 v107, v107, 0
	ds_read_b128 v[248:251], v121 offset:38912
	ds_read_b128 v[252:255], v121 offset:39936
	s_setprio 0
	s_waitcnt lgkmcnt(6)
	v_mfma_f32_16x16x32_bf16 v[80:83], v[224:227], v[32:35], v[80:83]
	v_pk_max_i16 v108, v108, 0
	v_mfma_f32_16x16x32_bf16 v[76:79], v[228:231], v[32:35], v[76:79]
	v_pk_max_i16 v109, v109, 0
	v_mfma_f32_16x16x32_bf16 v[72:75], v[228:231], v[36:39], v[72:75]
	v_pk_max_i16 v110, v110, 0
	v_mfma_f32_16x16x32_bf16 v[84:87], v[224:227], v[36:39], v[84:87]
	v_pk_max_i16 v111, v111, 0
	s_waitcnt lgkmcnt(4)
	v_mfma_f32_16x16x32_bf16 v[80:83], v[232:235], v[40:43], v[80:83]
	v_mfma_f32_16x16x32_bf16 v[76:79], v[236:239], v[40:43], v[76:79]
	v_mfma_f32_16x16x32_bf16 v[72:75], v[236:239], v[44:47], v[72:75]
	v_mfma_f32_16x16x32_bf16 v[84:87], v[232:235], v[44:47], v[84:87]
.Lnerf_hid_b2:
	s_waitcnt vmcnt(0) lgkmcnt(0)
	s_barrier
	ds_read_b128 v[224:227], v121 offset:40960
	ds_read_b128 v[228:231], v121 offset:41984
	ds_read_b128 v[64:67], v183 offset:512
	ds_read_b128 v[56:59], v183 offset:512
	ds_read_b128 v[68:71], v183 offset:576
	ds_read_b128 v[60:63], v183 offset:576
	v_mfma_f32_16x16x32_bf16 v[80:83], v[240:243], v[48:51], v[80:83]
	ds_read_b128 v[232:235], v121 offset:43008
	v_mfma_f32_16x16x32_bf16 v[76:79], v[244:247], v[48:51], v[76:79]
	ds_read_b128 v[236:239], v121 offset:44032
	v_mfma_f32_16x16x32_bf16 v[72:75], v[244:247], v[52:55], v[72:75]
	v_mfma_f32_16x16x32_bf16 v[84:87], v[240:243], v[52:55], v[84:87]
	ds_read_b128 v[240:243], v121 offset:45056
	ds_read_b128 v[244:247], v121 offset:46080
	v_mfma_f32_16x16x32_bf16 v[80:83], v[248:251], v[112:115], v[80:83]
	v_mfma_f32_16x16x32_bf16 v[76:79], v[252:255], v[112:115], v[76:79]
	v_mfma_f32_16x16x32_bf16 v[72:75], v[252:255], v[116:119], v[72:75]
	v_mfma_f32_16x16x32_bf16 v[84:87], v[248:251], v[116:119], v[84:87]
	ds_read_b128 v[248:251], v121 offset:47104
	ds_read_b128 v[252:255], v121 offset:48128
	s_setprio 3
	s_waitcnt lgkmcnt(6)
	v_mfma_f32_16x16x32_bf16 v[64:67], v[224:227], v[0:3], v[64:67]
	v_mfma_f32_16x16x32_bf16 v[68:71], v[228:231], v[0:3], v[68:71]
	v_mfma_f32_16x16x32_bf16 v[60:63], v[228:231], v[4:7], v[60:63]
	v_mfma_f32_16x16x32_bf16 v[56:59], v[224:227], v[4:7], v[56:59]
	ds_read_b128 v[224:227], v121 offset:49152
	ds_read_b128 v[228:231], v121 offset:50176
	s_waitcnt lgkmcnt(6)
	v_mfma_f32_16x16x32_bf16 v[64:67], v[232:235], v[12:15], v[64:67]
	v_cvt_pk_bf16_f32 v184, v80, v81
	v_mfma_f32_16x16x32_bf16 v[68:71], v[236:239], v[12:15], v[68:71]
	s_mov_b32 m0, s35
	s_add_i32 s51, s50, 0x10000
	v_cvt_pk_bf16_f32 v185, v82, v83
	v_mfma_f32_16x16x32_bf16 v[60:63], v[236:239], v[8:11], v[60:63]
	buffer_load_dwordx4 v125, s[36:39], s51 offen lds
	v_cvt_pk_bf16_f32 v186, v76, v77
	v_mfma_f32_16x16x32_bf16 v[56:59], v[232:235], v[8:11], v[56:59]
	v_cvt_pk_bf16_f32 v187, v78, v79
	ds_read_b128 v[232:235], v121 offset:51200
	ds_read_b128 v[236:239], v121 offset:52224
	s_waitcnt lgkmcnt(6)
	v_mfma_f32_16x16x32_bf16 v[64:67], v[240:243], v[16:19], v[64:67]
	v_cvt_pk_bf16_f32 v188, v84, v85
	v_mfma_f32_16x16x32_bf16 v[68:71], v[244:247], v[16:19], v[68:71]
	s_mov_b32 m0, s42
	s_add_i32 s51, s50, 0x12000
	v_cvt_pk_bf16_f32 v189, v86, v87
	v_mfma_f32_16x16x32_bf16 v[60:63], v[244:247], v[20:23], v[60:63]
	buffer_load_dwordx4 v125, s[36:39], s51 offen lds
	v_cvt_pk_bf16_f32 v190, v72, v73
	v_mfma_f32_16x16x32_bf16 v[56:59], v[240:243], v[20:23], v[56:59]
	v_cvt_pk_bf16_f32 v191, v74, v75
	ds_read_b128 v[240:243], v121 offset:53248
	ds_read_b128 v[244:247], v121 offset:54272
	s_waitcnt lgkmcnt(6)
	v_mfma_f32_16x16x32_bf16 v[64:67], v[248:251], v[24:27], v[64:67]
	v_pk_max_i16 v184, v184, 0
	v_mfma_f32_16x16x32_bf16 v[68:71], v[252:255], v[24:27], v[68:71]
	s_mov_b32 m0, s41
	s_add_i32 s51, s50, 0x14000
	v_pk_max_i16 v185, v185, 0
	v_mfma_f32_16x16x32_bf16 v[60:63], v[252:255], v[28:31], v[60:63]
	buffer_load_dwordx4 v125, s[36:39], s51 offen lds
	v_pk_max_i16 v186, v186, 0
	v_mfma_f32_16x16x32_bf16 v[56:59], v[248:251], v[28:31], v[56:59]
	v_pk_max_i16 v187, v187, 0
	ds_read_b128 v[248:251], v121 offset:55296
	ds_read_b128 v[252:255], v121 offset:56320
	s_setprio 2
	s_waitcnt lgkmcnt(6)
	v_mfma_f32_16x16x32_bf16 v[64:67], v[224:227], v[32:35], v[64:67]
	v_pk_max_i16 v188, v188, 0
	v_mfma_f32_16x16x32_bf16 v[68:71], v[228:231], v[32:35], v[68:71]
	s_mov_b32 m0, s40
	s_add_i32 s51, s50, 0x16000
	v_pk_max_i16 v189, v189, 0
	v_mfma_f32_16x16x32_bf16 v[60:63], v[228:231], v[36:39], v[60:63]
	buffer_load_dwordx4 v125, s[36:39], s51 offen lds
	v_pk_max_i16 v190, v190, 0
	v_mfma_f32_16x16x32_bf16 v[56:59], v[224:227], v[36:39], v[56:59]
	v_pk_max_i16 v191, v191, 0
	ds_read_b128 v[224:227], v121 offset:57344
	ds_read_b128 v[228:231], v121 offset:58368
	s_waitcnt lgkmcnt(6)
	v_mfma_f32_16x16x32_bf16 v[64:67], v[232:235], v[40:43], v[64:67]
	ds_read_b128 v[80:83], v183 offset:640
	ds_read_b128 v[84:87], v183 offset:640
	ds_read_b128 v[76:79], v183 offset:704
	ds_read_b128 v[72:75], v183 offset:704
	v_mfma_f32_16x16x32_bf16 v[68:71], v[236:239], v[40:43], v[68:71]
	v_mfma_f32_16x16x32_bf16 v[60:63], v[236:239], v[44:47], v[60:63]
	v_mfma_f32_16x16x32_bf16 v[56:59], v[232:235], v[44:47], v[56:59]
	ds_read_b128 v[232:235], v121 offset:59392
	ds_read_b128 v[236:239], v121 offset:60416
	s_waitcnt lgkmcnt(10)
	v_mfma_f32_16x16x32_bf16 v[64:67], v[240:243], v[48:51], v[64:67]
	v_mfma_f32_16x16x32_bf16 v[68:71], v[244:247], v[48:51], v[68:71]
	v_mfma_f32_16x16x32_bf16 v[60:63], v[244:247], v[52:55], v[60:63]
	v_mfma_f32_16x16x32_bf16 v[56:59], v[240:243], v[52:55], v[56:59]
	ds_read_b128 v[240:243], v121 offset:61440
	ds_read_b128 v[244:247], v121 offset:62464
	s_waitcnt lgkmcnt(10)
	v_mfma_f32_16x16x32_bf16 v[64:67], v[248:251], v[112:115], v[64:67]
	v_mfma_f32_16x16x32_bf16 v[68:71], v[252:255], v[112:115], v[68:71]
	v_mfma_f32_16x16x32_bf16 v[60:63], v[252:255], v[116:119], v[60:63]
	v_mfma_f32_16x16x32_bf16 v[56:59], v[248:251], v[116:119], v[56:59]
	ds_read_b128 v[248:251], v121 offset:63488
	ds_read_b128 v[252:255], v121 offset:64512
	s_setprio 1
	s_waitcnt lgkmcnt(6)
	v_mfma_f32_16x16x32_bf16 v[80:83], v[224:227], v[0:3], v[80:83]
	v_mfma_f32_16x16x32_bf16 v[76:79], v[228:231], v[0:3], v[76:79]
	v_mfma_f32_16x16x32_bf16 v[72:75], v[228:231], v[4:7], v[72:75]
	v_mfma_f32_16x16x32_bf16 v[84:87], v[224:227], v[4:7], v[84:87]
	ds_read_b128 v[224:227], v126 offset:57344
	ds_read_b128 v[228:231], v126 offset:58368
	s_waitcnt lgkmcnt(6)
	v_mfma_f32_16x16x32_bf16 v[80:83], v[232:235], v[12:15], v[80:83]
	v_cvt_pk_bf16_f32 v192, v64, v65
	v_mfma_f32_16x16x32_bf16 v[76:79], v[236:239], v[12:15], v[76:79]
	v_cvt_pk_bf16_f32 v193, v66, v67
	v_mfma_f32_16x16x32_bf16 v[72:75], v[236:239], v[8:11], v[72:75]
	v_cvt_pk_bf16_f32 v194, v68, v69
	v_mfma_f32_16x16x32_bf16 v[84:87], v[232:235], v[8:11], v[84:87]
	v_cvt_pk_bf16_f32 v195, v70, v71
	ds_read_b128 v[232:235], v126 offset:59392
	ds_read_b128 v[236:239], v126 offset:60416
	s_waitcnt lgkmcnt(6)
	v_mfma_f32_16x16x32_bf16 v[80:83], v[240:243], v[16:19], v[80:83]
	v_cvt_pk_bf16_f32 v196, v56, v57
	v_mfma_f32_16x16x32_bf16 v[76:79], v[244:247], v[16:19], v[76:79]
	v_cvt_pk_bf16_f32 v197, v58, v59
	v_mfma_f32_16x16x32_bf16 v[72:75], v[244:247], v[20:23], v[72:75]
	v_cvt_pk_bf16_f32 v198, v60, v61
	v_mfma_f32_16x16x32_bf16 v[84:87], v[240:243], v[20:23], v[84:87]
	v_cvt_pk_bf16_f32 v199, v62, v63
	ds_read_b128 v[240:243], v126 offset:61440
	ds_read_b128 v[244:247], v126 offset:62464
	s_waitcnt lgkmcnt(6)
	v_mfma_f32_16x16x32_bf16 v[80:83], v[248:251], v[24:27], v[80:83]
	v_pk_max_i16 v192, v192, 0
	v_mfma_f32_16x16x32_bf16 v[76:79], v[252:255], v[24:27], v[76:79]
	v_pk_max_i16 v193, v193, 0
	v_mfma_f32_16x16x32_bf16 v[72:75], v[252:255], v[28:31], v[72:75]
	v_pk_max_i16 v194, v194, 0
	v_mfma_f32_16x16x32_bf16 v[84:87], v[248:251], v[28:31], v[84:87]
	v_pk_max_i16 v195, v195, 0
	ds_read_b128 v[248:251], v126 offset:63488
	ds_read_b128 v[252:255], v126 offset:64512
	s_setprio 0
	s_waitcnt lgkmcnt(6)
	v_mfma_f32_16x16x32_bf16 v[80:83], v[224:227], v[32:35], v[80:83]
	v_pk_max_i16 v196, v196, 0
	v_mfma_f32_16x16x32_bf16 v[76:79], v[228:231], v[32:35], v[76:79]
	v_pk_max_i16 v197, v197, 0
	v_mfma_f32_16x16x32_bf16 v[72:75], v[228:231], v[36:39], v[72:75]
	v_pk_max_i16 v198, v198, 0
	v_mfma_f32_16x16x32_bf16 v[84:87], v[224:227], v[36:39], v[84:87]
	v_pk_max_i16 v199, v199, 0
	s_waitcnt lgkmcnt(4)
	v_mfma_f32_16x16x32_bf16 v[80:83], v[232:235], v[40:43], v[80:83]
	v_mfma_f32_16x16x32_bf16 v[76:79], v[236:239], v[40:43], v[76:79]
	v_mfma_f32_16x16x32_bf16 v[72:75], v[236:239], v[44:47], v[72:75]
	v_mfma_f32_16x16x32_bf16 v[84:87], v[232:235], v[44:47], v[84:87]
.Lnerf_hid_b3:
	s_waitcnt vmcnt(0) lgkmcnt(0)
	s_barrier
	ds_read_b128 v[224:227], v121 offset:8192
	ds_read_b128 v[228:231], v121 offset:9216
	ds_read_b128 v[64:67], v183 offset:768
	ds_read_b128 v[56:59], v183 offset:768
	ds_read_b128 v[68:71], v183 offset:832
	ds_read_b128 v[60:63], v183 offset:832
	v_mfma_f32_16x16x32_bf16 v[80:83], v[240:243], v[48:51], v[80:83]
	ds_read_b128 v[232:235], v121 offset:10240
	v_mfma_f32_16x16x32_bf16 v[76:79], v[244:247], v[48:51], v[76:79]
	ds_read_b128 v[236:239], v121 offset:11264
	v_mfma_f32_16x16x32_bf16 v[72:75], v[244:247], v[52:55], v[72:75]
	v_mfma_f32_16x16x32_bf16 v[84:87], v[240:243], v[52:55], v[84:87]
	ds_read_b128 v[240:243], v121 offset:12288
	ds_read_b128 v[244:247], v121 offset:13312
	v_mfma_f32_16x16x32_bf16 v[80:83], v[248:251], v[112:115], v[80:83]
	v_mfma_f32_16x16x32_bf16 v[76:79], v[252:255], v[112:115], v[76:79]
	v_mfma_f32_16x16x32_bf16 v[72:75], v[252:255], v[116:119], v[72:75]
	v_mfma_f32_16x16x32_bf16 v[84:87], v[248:251], v[116:119], v[84:87]
	ds_read_b128 v[248:251], v121 offset:14336
	ds_read_b128 v[252:255], v121 offset:15360
	s_setprio 3
	s_waitcnt lgkmcnt(6)
	v_mfma_f32_16x16x32_bf16 v[64:67], v[224:227], v[0:3], v[64:67]
	v_mfma_f32_16x16x32_bf16 v[68:71], v[228:231], v[0:3], v[68:71]
	v_mfma_f32_16x16x32_bf16 v[60:63], v[228:231], v[4:7], v[60:63]
	v_mfma_f32_16x16x32_bf16 v[56:59], v[224:227], v[4:7], v[56:59]
	ds_read_b128 v[224:227], v121 offset:16384
	ds_read_b128 v[228:231], v121 offset:17408
	s_waitcnt lgkmcnt(6)
	v_mfma_f32_16x16x32_bf16 v[64:67], v[232:235], v[12:15], v[64:67]
	v_cvt_pk_bf16_f32 v200, v80, v81
	v_mfma_f32_16x16x32_bf16 v[68:71], v[236:239], v[12:15], v[68:71]
	s_mov_b32 m0, s28
	s_add_i32 s51, s50, 0x18000
	v_cvt_pk_bf16_f32 v201, v82, v83
	v_mfma_f32_16x16x32_bf16 v[60:63], v[236:239], v[8:11], v[60:63]
	buffer_load_dwordx4 v125, s[36:39], s51 offen lds
	v_cvt_pk_bf16_f32 v202, v76, v77
	v_mfma_f32_16x16x32_bf16 v[56:59], v[232:235], v[8:11], v[56:59]
	v_cvt_pk_bf16_f32 v203, v78, v79
	ds_read_b128 v[232:235], v121 offset:18432
	ds_read_b128 v[236:239], v121 offset:19456
	s_waitcnt lgkmcnt(6)
	v_mfma_f32_16x16x32_bf16 v[64:67], v[240:243], v[16:19], v[64:67]
	v_cvt_pk_bf16_f32 v204, v84, v85
	v_mfma_f32_16x16x32_bf16 v[68:71], v[244:247], v[16:19], v[68:71]
	s_mov_b32 m0, s29
	s_add_i32 s51, s50, 0x1a000
	v_cvt_pk_bf16_f32 v205, v86, v87
	v_mfma_f32_16x16x32_bf16 v[60:63], v[244:247], v[20:23], v[60:63]
	buffer_load_dwordx4 v125, s[36:39], s51 offen lds
	v_cvt_pk_bf16_f32 v206, v72, v73
	v_mfma_f32_16x16x32_bf16 v[56:59], v[240:243], v[20:23], v[56:59]
	v_cvt_pk_bf16_f32 v207, v74, v75
	ds_read_b128 v[240:243], v121 offset:20480
	ds_read_b128 v[244:247], v121 offset:21504
	s_waitcnt lgkmcnt(6)
	v_mfma_f32_16x16x32_bf16 v[64:67], v[248:251], v[24:27], v[64:67]
	v_pk_max_i16 v200, v200, 0
	v_mfma_f32_16x16x32_bf16 v[68:71], v[252:255], v[24:27], v[68:71]
	s_mov_b32 m0, s33
	s_add_i32 s51, s50, 0x1c000
	v_pk_max_i16 v201, v201, 0
	v_mfma_f32_16x16x32_bf16 v[60:63], v[252:255], v[28:31], v[60:63]
	buffer_load_dwordx4 v125, s[36:39], s51 offen lds
	v_pk_max_i16 v202, v202, 0
	v_mfma_f32_16x16x32_bf16 v[56:59], v[248:251], v[28:31], v[56:59]
	v_pk_max_i16 v203, v203, 0
	ds_read_b128 v[248:251], v121 offset:22528
	ds_read_b128 v[252:255], v121 offset:23552
	s_setprio 2
	s_waitcnt lgkmcnt(6)
	v_mfma_f32_16x16x32_bf16 v[64:67], v[224:227], v[32:35], v[64:67]
	v_pk_max_i16 v204, v204, 0
	v_mfma_f32_16x16x32_bf16 v[68:71], v[228:231], v[32:35], v[68:71]
	s_mov_b32 m0, s34
	s_add_i32 s51, s50, 0x1e000
	v_pk_max_i16 v205, v205, 0
	v_mfma_f32_16x16x32_bf16 v[60:63], v[228:231], v[36:39], v[60:63]
	buffer_load_dwordx4 v125, s[36:39], s51 offen lds
	v_pk_max_i16 v206, v206, 0
	v_mfma_f32_16x16x32_bf16 v[56:59], v[224:227], v[36:39], v[56:59]
	v_pk_max_i16 v207, v207, 0
	ds_read_b128 v[224:227], v121 offset:24576
	ds_read_b128 v[228:231], v121 offset:25600
	s_waitcnt lgkmcnt(6)
	v_mfma_f32_16x16x32_bf16 v[64:67], v[232:235], v[40:43], v[64:67]
	ds_read_b128 v[80:83], v183 offset:896
	ds_read_b128 v[84:87], v183 offset:896
	ds_read_b128 v[76:79], v183 offset:960
	ds_read_b128 v[72:75], v183 offset:960
	v_mfma_f32_16x16x32_bf16 v[68:71], v[236:239], v[40:43], v[68:71]
	v_mfma_f32_16x16x32_bf16 v[60:63], v[236:239], v[44:47], v[60:63]
	v_mfma_f32_16x16x32_bf16 v[56:59], v[232:235], v[44:47], v[56:59]
	ds_read_b128 v[232:235], v121 offset:26624
	ds_read_b128 v[236:239], v121 offset:27648
	s_waitcnt lgkmcnt(10)
	v_mfma_f32_16x16x32_bf16 v[64:67], v[240:243], v[48:51], v[64:67]
	v_mfma_f32_16x16x32_bf16 v[68:71], v[244:247], v[48:51], v[68:71]
	v_mfma_f32_16x16x32_bf16 v[60:63], v[244:247], v[52:55], v[60:63]
	v_mfma_f32_16x16x32_bf16 v[56:59], v[240:243], v[52:55], v[56:59]
	ds_read_b128 v[240:243], v121 offset:28672
	ds_read_b128 v[244:247], v121 offset:29696
	s_waitcnt lgkmcnt(10)
	v_mfma_f32_16x16x32_bf16 v[64:67], v[248:251], v[112:115], v[64:67]
	v_mfma_f32_16x16x32_bf16 v[68:71], v[252:255], v[112:115], v[68:71]
	v_mfma_f32_16x16x32_bf16 v[60:63], v[252:255], v[116:119], v[60:63]
	v_mfma_f32_16x16x32_bf16 v[56:59], v[248:251], v[116:119], v[56:59]
	ds_read_b128 v[248:251], v121 offset:30720
	ds_read_b128 v[252:255], v121 offset:31744
	s_setprio 1
	s_waitcnt lgkmcnt(6)
	v_mfma_f32_16x16x32_bf16 v[80:83], v[224:227], v[0:3], v[80:83]
	v_mfma_f32_16x16x32_bf16 v[76:79], v[228:231], v[0:3], v[76:79]
	v_mfma_f32_16x16x32_bf16 v[72:75], v[228:231], v[4:7], v[72:75]
	v_mfma_f32_16x16x32_bf16 v[84:87], v[224:227], v[4:7], v[84:87]
	ds_read_b128 v[224:227], v121 offset:32768
	ds_read_b128 v[228:231], v121 offset:33792
	s_waitcnt lgkmcnt(6)
	v_mfma_f32_16x16x32_bf16 v[80:83], v[232:235], v[12:15], v[80:83]
	v_cvt_pk_bf16_f32 v208, v64, v65
	v_mfma_f32_16x16x32_bf16 v[76:79], v[236:239], v[12:15], v[76:79]
	v_cvt_pk_bf16_f32 v209, v66, v67
	v_mfma_f32_16x16x32_bf16 v[72:75], v[236:239], v[8:11], v[72:75]
	v_cvt_pk_bf16_f32 v210, v68, v69
	v_mfma_f32_16x16x32_bf16 v[84:87], v[232:235], v[8:11], v[84:87]
	v_cvt_pk_bf16_f32 v211, v70, v71
	ds_read_b128 v[232:235], v121 offset:34816
	ds_read_b128 v[236:239], v121 offset:35840
	s_waitcnt lgkmcnt(6)
	v_mfma_f32_16x16x32_bf16 v[80:83], v[240:243], v[16:19], v[80:83]
	v_cvt_pk_bf16_f32 v212, v56, v57
	v_mfma_f32_16x16x32_bf16 v[76:79], v[244:247], v[16:19], v[76:79]
	v_cvt_pk_bf16_f32 v213, v58, v59
	v_mfma_f32_16x16x32_bf16 v[72:75], v[244:247], v[20:23], v[72:75]
	v_cvt_pk_bf16_f32 v214, v60, v61
	v_mfma_f32_16x16x32_bf16 v[84:87], v[240:243], v[20:23], v[84:87]
	v_cvt_pk_bf16_f32 v215, v62, v63
	ds_read_b128 v[240:243], v121 offset:36864
	ds_read_b128 v[244:247], v121 offset:37888
	s_waitcnt lgkmcnt(6)
	v_mfma_f32_16x16x32_bf16 v[80:83], v[248:251], v[24:27], v[80:83]
	v_pk_max_i16 v208, v208, 0
	v_mfma_f32_16x16x32_bf16 v[76:79], v[252:255], v[24:27], v[76:79]
	v_pk_max_i16 v209, v209, 0
	v_mfma_f32_16x16x32_bf16 v[72:75], v[252:255], v[28:31], v[72:75]
	v_pk_max_i16 v210, v210, 0
	v_mfma_f32_16x16x32_bf16 v[84:87], v[248:251], v[28:31], v[84:87]
	v_pk_max_i16 v211, v211, 0
	ds_read_b128 v[248:251], v121 offset:38912
	ds_read_b128 v[252:255], v121 offset:39936
	s_setprio 0
	s_waitcnt lgkmcnt(6)
	v_mfma_f32_16x16x32_bf16 v[80:83], v[224:227], v[32:35], v[80:83]
	v_pk_max_i16 v212, v212, 0
	v_mfma_f32_16x16x32_bf16 v[76:79], v[228:231], v[32:35], v[76:79]
	v_pk_max_i16 v213, v213, 0
	v_mfma_f32_16x16x32_bf16 v[72:75], v[228:231], v[36:39], v[72:75]
	v_pk_max_i16 v214, v214, 0
	v_mfma_f32_16x16x32_bf16 v[84:87], v[224:227], v[36:39], v[84:87]
	v_pk_max_i16 v215, v215, 0
	s_waitcnt lgkmcnt(4)
	v_mfma_f32_16x16x32_bf16 v[80:83], v[232:235], v[40:43], v[80:83]
	v_mfma_f32_16x16x32_bf16 v[76:79], v[236:239], v[40:43], v[76:79]
	v_mfma_f32_16x16x32_bf16 v[72:75], v[236:239], v[44:47], v[72:75]
	v_mfma_f32_16x16x32_bf16 v[84:87], v[232:235], v[44:47], v[84:87]
	s_cmp_eq_u32 s52, 3
	s_cbranch_scc1 .Lnerf_head
.Lnerf_hid_b4:
	s_waitcnt vmcnt(0) lgkmcnt(0)
	s_barrier
	ds_read_b128 v[224:227], v121 offset:40960
	ds_read_b128 v[228:231], v121 offset:41984
	ds_read_b128 v[64:67], v183 offset:1024
	ds_read_b128 v[56:59], v183 offset:1024
	ds_read_b128 v[68:71], v183 offset:1088
	ds_read_b128 v[60:63], v183 offset:1088
	v_mfma_f32_16x16x32_bf16 v[80:83], v[240:243], v[48:51], v[80:83]
	ds_read_b128 v[232:235], v121 offset:43008
	v_mfma_f32_16x16x32_bf16 v[76:79], v[244:247], v[48:51], v[76:79]
	ds_read_b128 v[236:239], v121 offset:44032
	v_mfma_f32_16x16x32_bf16 v[72:75], v[244:247], v[52:55], v[72:75]
	v_mfma_f32_16x16x32_bf16 v[84:87], v[240:243], v[52:55], v[84:87]
	ds_read_b128 v[240:243], v121 offset:45056
	ds_read_b128 v[244:247], v121 offset:46080
	v_mfma_f32_16x16x32_bf16 v[80:83], v[248:251], v[112:115], v[80:83]
	v_mfma_f32_16x16x32_bf16 v[76:79], v[252:255], v[112:115], v[76:79]
	v_mfma_f32_16x16x32_bf16 v[72:75], v[252:255], v[116:119], v[72:75]
	v_mfma_f32_16x16x32_bf16 v[84:87], v[248:251], v[116:119], v[84:87]
	ds_read_b128 v[248:251], v121 offset:47104
	ds_read_b128 v[252:255], v121 offset:48128
	s_setprio 3
	s_waitcnt lgkmcnt(6)
	v_mfma_f32_16x16x32_bf16 v[64:67], v[224:227], v[88:91], v[64:67]
	v_mfma_f32_16x16x32_bf16 v[68:71], v[228:231], v[88:91], v[68:71]
	v_mfma_f32_16x16x32_bf16 v[60:63], v[228:231], v[92:95], v[60:63]
	v_mfma_f32_16x16x32_bf16 v[56:59], v[224:227], v[92:95], v[56:59]
	ds_read_b128 v[224:227], v121 offset:49152
	ds_read_b128 v[228:231], v121 offset:50176
	s_waitcnt lgkmcnt(6)
	v_mfma_f32_16x16x32_bf16 v[64:67], v[232:235], v[96:99], v[64:67]
	v_cvt_pk_bf16_f32 v216, v80, v81
	v_mfma_f32_16x16x32_bf16 v[68:71], v[236:239], v[96:99], v[68:71]
	s_mov_b32 m0, s35
	s_add_i32 s51, s50, 0x20000
	v_cvt_pk_bf16_f32 v217, v82, v83
	v_mfma_f32_16x16x32_bf16 v[60:63], v[236:239], v[100:103], v[60:63]
	buffer_load_dwordx4 v125, s[36:39], s51 offen lds
	v_cvt_pk_bf16_f32 v218, v76, v77
	v_mfma_f32_16x16x32_bf16 v[56:59], v[232:235], v[100:103], v[56:59]
	v_cvt_pk_bf16_f32 v219, v78, v79
	ds_read_b128 v[232:235], v121 offset:51200
	ds_read_b128 v[236:239], v121 offset:52224
	s_waitcnt lgkmcnt(6)
	v_mfma_f32_16x16x32_bf16 v[64:67], v[240:243], v[104:107], v[64:67]
	v_cvt_pk_bf16_f32 v220, v84, v85
	v_mfma_f32_16x16x32_bf16 v[68:71], v[244:247], v[104:107], v[68:71]
	s_mov_b32 m0, s42
	s_add_i32 s51, s50, 0x22000
	v_cvt_pk_bf16_f32 v221, v86, v87
	v_mfma_f32_16x16x32_bf16 v[60:63], v[244:247], v[108:111], v[60:63]
	buffer_load_dwordx4 v125, s[36:39], s51 offen lds
	v_cvt_pk_bf16_f32 v222, v72, v73
	v_mfma_f32_16x16x32_bf16 v[56:59], v[240:243], v[108:111], v[56:59]
	v_cvt_pk_bf16_f32 v223, v74, v75
	ds_read_b128 v[240:243], v121 offset:53248
	ds_read_b128 v[244:247], v121 offset:54272
	s_waitcnt lgkmcnt(6)
	v_mfma_f32_16x16x32_bf16 v[64:67], v[248:251], v[184:187], v[64:67]
	v_pk_max_i16 v216, v216, 0
	v_mfma_f32_16x16x32_bf16 v[68:71], v[252:255], v[184:187], v[68:71]
	s_mov_b32 m0, s41
	s_add_i32 s51, s50, 0x24000
	v_pk_max_i16 v217, v217, 0
	v_mfma_f32_16x16x32_bf16 v[60:63], v[252:255], v[188:191], v[60:63]
	buffer_load_dwordx4 v125, s[36:39], s51 offen lds
	v_pk_max_i16 v218, v218, 0
	v_mfma_f32_16x16x32_bf16 v[56:59], v[248:251], v[188:191], v[56:59]
	v_pk_max_i16 v219, v219, 0
	ds_read_b128 v[248:251], v121 offset:55296
	ds_read_b128 v[252:255], v121 offset:56320
	s_setprio 2
	s_waitcnt lgkmcnt(6)
	v_mfma_f32_16x16x32_bf16 v[64:67], v[224:227], v[192:195], v[64:67]
	v_pk_max_i16 v220, v220, 0
	v_mfma_f32_16x16x32_bf16 v[68:71], v[228:231], v[192:195], v[68:71]
	s_mov_b32 m0, s40
	s_add_i32 s51, s50, 0x26000
	v_pk_max_i16 v221, v221, 0
	v_mfma_f32_16x16x32_bf16 v[60:63], v[228:231], v[196:199], v[60:63]
	buffer_load_dwordx4 v125, s[36:39], s51 offen lds
	v_pk_max_i16 v222, v222, 0
	v_mfma_f32_16x16x32_bf16 v[56:59], v[224:227], v[196:199], v[56:59]
	v_pk_max_i16 v223, v223, 0
	ds_read_b128 v[224:227], v121 offset:57344
	ds_read_b128 v[228:231], v121 offset:58368
	s_waitcnt lgkmcnt(6)
	v_mfma_f32_16x16x32_bf16 v[64:67], v[232:235], v[200:203], v[64:67]
	ds_read_b128 v[80:83], v183 offset:1152
	ds_read_b128 v[84:87], v183 offset:1152
	ds_read_b128 v[76:79], v183 offset:1216
	ds_read_b128 v[72:75], v183 offset:1216
	v_mfma_f32_16x16x32_bf16 v[68:71], v[236:239], v[200:203], v[68:71]
	v_mfma_f32_16x16x32_bf16 v[60:63], v[236:239], v[204:207], v[60:63]
	v_mfma_f32_16x16x32_bf16 v[56:59], v[232:235], v[204:207], v[56:59]
	ds_read_b128 v[232:235], v121 offset:59392
	ds_read_b128 v[236:239], v121 offset:60416
	s_waitcnt lgkmcnt(10)
	v_mfma_f32_16x16x32_bf16 v[64:67], v[240:243], v[208:211], v[64:67]
	v_mfma_f32_16x16x32_bf16 v[68:71], v[244:247], v[208:211], v[68:71]
	v_mfma_f32_16x16x32_bf16 v[60:63], v[244:247], v[212:215], v[60:63]
	v_mfma_f32_16x16x32_bf16 v[56:59], v[240:243], v[212:215], v[56:59]
	ds_read_b128 v[240:243], v121 offset:61440
	ds_read_b128 v[244:247], v121 offset:62464
	s_waitcnt lgkmcnt(10)
	v_mfma_f32_16x16x32_bf16 v[64:67], v[248:251], v[216:219], v[64:67]
	v_mfma_f32_16x16x32_bf16 v[68:71], v[252:255], v[216:219], v[68:71]
	v_mfma_f32_16x16x32_bf16 v[60:63], v[252:255], v[220:223], v[60:63]
	v_mfma_f32_16x16x32_bf16 v[56:59], v[248:251], v[220:223], v[56:59]
	ds_read_b128 v[248:251], v121 offset:63488
	ds_read_b128 v[252:255], v121 offset:64512
	s_setprio 1
	s_waitcnt lgkmcnt(6)
	v_mfma_f32_16x16x32_bf16 v[80:83], v[224:227], v[88:91], v[80:83]
	v_mfma_f32_16x16x32_bf16 v[76:79], v[228:231], v[88:91], v[76:79]
	v_mfma_f32_16x16x32_bf16 v[72:75], v[228:231], v[92:95], v[72:75]
	v_mfma_f32_16x16x32_bf16 v[84:87], v[224:227], v[92:95], v[84:87]
	ds_read_b128 v[224:227], v126 offset:57344
	ds_read_b128 v[228:231], v126 offset:58368
	s_waitcnt lgkmcnt(6)
	v_mfma_f32_16x16x32_bf16 v[80:83], v[232:235], v[96:99], v[80:83]
	v_cvt_pk_bf16_f32 v0, v64, v65
	v_mfma_f32_16x16x32_bf16 v[76:79], v[236:239], v[96:99], v[76:79]
	v_cvt_pk_bf16_f32 v1, v66, v67
	v_mfma_f32_16x16x32_bf16 v[72:75], v[236:239], v[100:103], v[72:75]
	v_cvt_pk_bf16_f32 v2, v68, v69
	v_mfma_f32_16x16x32_bf16 v[84:87], v[232:235], v[100:103], v[84:87]
	v_cvt_pk_bf16_f32 v3, v70, v71
	ds_read_b128 v[232:235], v126 offset:59392
	ds_read_b128 v[236:239], v126 offset:60416
	s_waitcnt lgkmcnt(6)
	v_mfma_f32_16x16x32_bf16 v[80:83], v[240:243], v[104:107], v[80:83]
	v_cvt_pk_bf16_f32 v4, v56, v57
	v_mfma_f32_16x16x32_bf16 v[76:79], v[244:247], v[104:107], v[76:79]
	v_cvt_pk_bf16_f32 v5, v58, v59
	v_mfma_f32_16x16x32_bf16 v[72:75], v[244:247], v[108:111], v[72:75]
	v_cvt_pk_bf16_f32 v6, v60, v61
	v_mfma_f32_16x16x32_bf16 v[84:87], v[240:243], v[108:111], v[84:87]
	v_cvt_pk_bf16_f32 v7, v62, v63
	ds_read_b128 v[240:243], v126 offset:61440
	ds_read_b128 v[244:247], v126 offset:62464
	s_waitcnt lgkmcnt(6)
	v_mfma_f32_16x16x32_bf16 v[80:83], v[248:251], v[184:187], v[80:83]
	v_pk_max_i16 v0, v0, 0
	v_mfma_f32_16x16x32_bf16 v[76:79], v[252:255], v[184:187], v[76:79]
	v_pk_max_i16 v1, v1, 0
	v_mfma_f32_16x16x32_bf16 v[72:75], v[252:255], v[188:191], v[72:75]
	v_pk_max_i16 v2, v2, 0
	v_mfma_f32_16x16x32_bf16 v[84:87], v[248:251], v[188:191], v[84:87]
	v_pk_max_i16 v3, v3, 0
	ds_read_b128 v[248:251], v126 offset:63488
	ds_read_b128 v[252:255], v126 offset:64512
	s_setprio 0
	s_waitcnt lgkmcnt(6)
	v_mfma_f32_16x16x32_bf16 v[80:83], v[224:227], v[192:195], v[80:83]
	v_pk_max_i16 v4, v4, 0
	v_mfma_f32_16x16x32_bf16 v[76:79], v[228:231], v[192:195], v[76:79]
	v_pk_max_i16 v5, v5, 0
	v_mfma_f32_16x16x32_bf16 v[72:75], v[228:231], v[196:199], v[72:75]
	v_pk_max_i16 v6, v6, 0
	v_mfma_f32_16x16x32_bf16 v[84:87], v[224:227], v[196:199], v[84:87]
	v_pk_max_i16 v7, v7, 0
	s_waitcnt lgkmcnt(4)
	v_mfma_f32_16x16x32_bf16 v[80:83], v[232:235], v[200:203], v[80:83]
	v_mfma_f32_16x16x32_bf16 v[76:79], v[236:239], v[200:203], v[76:79]
	v_mfma_f32_16x16x32_bf16 v[72:75], v[236:239], v[204:207], v[72:75]
	v_mfma_f32_16x16x32_bf16 v[84:87], v[232:235], v[204:207], v[84:87]
.Lnerf_hid_b5:
	s_waitcnt vmcnt(0) lgkmcnt(0)
	s_barrier
	ds_read_b128 v[224:227], v121 offset:8192
	ds_read_b128 v[228:231], v121 offset:9216
	ds_read_b128 v[64:67], v183 offset:1280
	ds_read_b128 v[56:59], v183 offset:1280
	ds_read_b128 v[68:71], v183 offset:1344
	ds_read_b128 v[60:63], v183 offset:1344
	v_mfma_f32_16x16x32_bf16 v[80:83], v[240:243], v[208:211], v[80:83]
	ds_read_b128 v[232:235], v121 offset:10240
	v_mfma_f32_16x16x32_bf16 v[76:79], v[244:247], v[208:211], v[76:79]
	ds_read_b128 v[236:239], v121 offset:11264
	v_mfma_f32_16x16x32_bf16 v[72:75], v[244:247], v[212:215], v[72:75]
	v_mfma_f32_16x16x32_bf16 v[84:87], v[240:243], v[212:215], v[84:87]
	ds_read_b128 v[240:243], v121 offset:12288
	ds_read_b128 v[244:247], v121 offset:13312
	v_mfma_f32_16x16x32_bf16 v[80:83], v[248:251], v[216:219], v[80:83]
	v_mfma_f32_16x16x32_bf16 v[76:79], v[252:255], v[216:219], v[76:79]
	v_mfma_f32_16x16x32_bf16 v[72:75], v[252:255], v[220:223], v[72:75]
	v_mfma_f32_16x16x32_bf16 v[84:87], v[248:251], v[220:223], v[84:87]
	ds_read_b128 v[248:251], v121 offset:14336
	ds_read_b128 v[252:255], v121 offset:15360
	s_setprio 3
	s_waitcnt lgkmcnt(6)
	v_mfma_f32_16x16x32_bf16 v[64:67], v[224:227], v[88:91], v[64:67]
	v_mfma_f32_16x16x32_bf16 v[68:71], v[228:231], v[88:91], v[68:71]
	v_mfma_f32_16x16x32_bf16 v[60:63], v[228:231], v[92:95], v[60:63]
	v_mfma_f32_16x16x32_bf16 v[56:59], v[224:227], v[92:95], v[56:59]
	ds_read_b128 v[224:227], v121 offset:16384
	ds_read_b128 v[228:231], v121 offset:17408
	s_waitcnt lgkmcnt(6)
	v_mfma_f32_16x16x32_bf16 v[64:67], v[232:235], v[96:99], v[64:67]
	v_cvt_pk_bf16_f32 v12, v80, v81
	v_mfma_f32_16x16x32_bf16 v[68:71], v[236:239], v[96:99], v[68:71]
	s_mov_b32 m0, s28
	s_add_i32 s51, s50, 0x28000
	v_cvt_pk_bf16_f32 v13, v82, v83
	v_mfma_f32_16x16x32_bf16 v[60:63], v[236:239], v[100:103], v[60:63]
	buffer_load_dwordx4 v125, s[36:39], s51 offen lds
	v_cvt_pk_bf16_f32 v14, v76, v77
	v_mfma_f32_16x16x32_bf16 v[56:59], v[232:235], v[100:103], v[56:59]
	v_cvt_pk_bf16_f32 v15, v78, v79
	ds_read_b128 v[232:235], v121 offset:18432
	ds_read_b128 v[236:239], v121 offset:19456
	s_waitcnt lgkmcnt(6)
	v_mfma_f32_16x16x32_bf16 v[64:67], v[240:243], v[104:107], v[64:67]
	v_cvt_pk_bf16_f32 v8, v84, v85
	v_mfma_f32_16x16x32_bf16 v[68:71], v[244:247], v[104:107], v[68:71]
	s_mov_b32 m0, s29
	s_add_i32 s51, s50, 0x2a000
	v_cvt_pk_bf16_f32 v9, v86, v87
	v_mfma_f32_16x16x32_bf16 v[60:63], v[244:247], v[108:111], v[60:63]
	buffer_load_dwordx4 v125, s[36:39], s51 offen lds
	v_cvt_pk_bf16_f32 v10, v72, v73
	v_mfma_f32_16x16x32_bf16 v[56:59], v[240:243], v[108:111], v[56:59]
	v_cvt_pk_bf16_f32 v11, v74, v75
	ds_read_b128 v[240:243], v121 offset:20480
	ds_read_b128 v[244:247], v121 offset:21504
	s_waitcnt lgkmcnt(6)
	v_mfma_f32_16x16x32_bf16 v[64:67], v[248:251], v[184:187], v[64:67]
	v_pk_max_i16 v12, v12, 0
	v_mfma_f32_16x16x32_bf16 v[68:71], v[252:255], v[184:187], v[68:71]
	s_mov_b32 m0, s33
	s_add_i32 s51, s50, 0x2c000
	v_pk_max_i16 v13, v13, 0
	v_mfma_f32_16x16x32_bf16 v[60:63], v[252:255], v[188:191], v[60:63]
	buffer_load_dwordx4 v125, s[36:39], s51 offen lds
	v_pk_max_i16 v14, v14, 0
	v_mfma_f32_16x16x32_bf16 v[56:59], v[248:251], v[188:191], v[56:59]
	v_pk_max_i16 v15, v15, 0
	ds_read_b128 v[248:251], v121 offset:22528
	ds_read_b128 v[252:255], v121 offset:23552
	s_setprio 2
	s_waitcnt lgkmcnt(6)
	v_mfma_f32_16x16x32_bf16 v[64:67], v[224:227], v[192:195], v[64:67]
	v_pk_max_i16 v8, v8, 0
	v_mfma_f32_16x16x32_bf16 v[68:71], v[228:231], v[192:195], v[68:71]
	s_mov_b32 m0, s34
	s_add_i32 s51, s50, 0x2e000
	v_pk_max_i16 v9, v9, 0
	v_mfma_f32_16x16x32_bf16 v[60:63], v[228:231], v[196:199], v[60:63]
	buffer_load_dwordx4 v125, s[36:39], s51 offen lds
	v_pk_max_i16 v10, v10, 0
	v_mfma_f32_16x16x32_bf16 v[56:59], v[224:227], v[196:199], v[56:59]
	v_pk_max_i16 v11, v11, 0
	ds_read_b128 v[224:227], v121 offset:24576
	ds_read_b128 v[228:231], v121 offset:25600
	s_waitcnt lgkmcnt(6)
	v_mfma_f32_16x16x32_bf16 v[64:67], v[232:235], v[200:203], v[64:67]
	ds_read_b128 v[80:83], v183 offset:1408
	ds_read_b128 v[84:87], v183 offset:1408
	ds_read_b128 v[76:79], v183 offset:1472
	ds_read_b128 v[72:75], v183 offset:1472
	v_mfma_f32_16x16x32_bf16 v[68:71], v[236:239], v[200:203], v[68:71]
	v_mfma_f32_16x16x32_bf16 v[60:63], v[236:239], v[204:207], v[60:63]
	v_mfma_f32_16x16x32_bf16 v[56:59], v[232:235], v[204:207], v[56:59]
	ds_read_b128 v[232:235], v121 offset:26624
	ds_read_b128 v[236:239], v121 offset:27648
	s_waitcnt lgkmcnt(10)
	v_mfma_f32_16x16x32_bf16 v[64:67], v[240:243], v[208:211], v[64:67]
	v_mfma_f32_16x16x32_bf16 v[68:71], v[244:247], v[208:211], v[68:71]
	v_mfma_f32_16x16x32_bf16 v[60:63], v[244:247], v[212:215], v[60:63]
	v_mfma_f32_16x16x32_bf16 v[56:59], v[240:243], v[212:215], v[56:59]
	ds_read_b128 v[240:243], v121 offset:28672
	ds_read_b128 v[244:247], v121 offset:29696
	s_waitcnt lgkmcnt(10)
	v_mfma_f32_16x16x32_bf16 v[64:67], v[248:251], v[216:219], v[64:67]
	v_mfma_f32_16x16x32_bf16 v[68:71], v[252:255], v[216:219], v[68:71]
	v_mfma_f32_16x16x32_bf16 v[60:63], v[252:255], v[220:223], v[60:63]
	v_mfma_f32_16x16x32_bf16 v[56:59], v[248:251], v[220:223], v[56:59]
	ds_read_b128 v[248:251], v121 offset:30720
	ds_read_b128 v[252:255], v121 offset:31744
	s_setprio 1
	s_waitcnt lgkmcnt(6)
	v_mfma_f32_16x16x32_bf16 v[80:83], v[224:227], v[88:91], v[80:83]
	v_mfma_f32_16x16x32_bf16 v[76:79], v[228:231], v[88:91], v[76:79]
	v_mfma_f32_16x16x32_bf16 v[72:75], v[228:231], v[92:95], v[72:75]
	v_mfma_f32_16x16x32_bf16 v[84:87], v[224:227], v[92:95], v[84:87]
	ds_read_b128 v[224:227], v121 offset:32768
	ds_read_b128 v[228:231], v121 offset:33792
	s_waitcnt lgkmcnt(6)
	v_mfma_f32_16x16x32_bf16 v[80:83], v[232:235], v[96:99], v[80:83]
	v_cvt_pk_bf16_f32 v16, v64, v65
	v_mfma_f32_16x16x32_bf16 v[76:79], v[236:239], v[96:99], v[76:79]
	v_cvt_pk_bf16_f32 v17, v66, v67
	v_mfma_f32_16x16x32_bf16 v[72:75], v[236:239], v[100:103], v[72:75]
	v_cvt_pk_bf16_f32 v18, v68, v69
	v_mfma_f32_16x16x32_bf16 v[84:87], v[232:235], v[100:103], v[84:87]
	v_cvt_pk_bf16_f32 v19, v70, v71
	ds_read_b128 v[232:235], v121 offset:34816
	ds_read_b128 v[236:239], v121 offset:35840
	s_waitcnt lgkmcnt(6)
	v_mfma_f32_16x16x32_bf16 v[80:83], v[240:243], v[104:107], v[80:83]
	v_cvt_pk_bf16_f32 v20, v56, v57
	v_mfma_f32_16x16x32_bf16 v[76:79], v[244:247], v[104:107], v[76:79]
	v_cvt_pk_bf16_f32 v21, v58, v59
	v_mfma_f32_16x16x32_bf16 v[72:75], v[244:247], v[108:111], v[72:75]
	v_cvt_pk_bf16_f32 v22, v60, v61
	v_mfma_f32_16x16x32_bf16 v[84:87], v[240:243], v[108:111], v[84:87]
	v_cvt_pk_bf16_f32 v23, v62, v63
	ds_read_b128 v[240:243], v121 offset:36864
	ds_read_b128 v[244:247], v121 offset:37888
	s_waitcnt lgkmcnt(6)
	v_mfma_f32_16x16x32_bf16 v[80:83], v[248:251], v[184:187], v[80:83]
	v_pk_max_i16 v16, v16, 0
	v_mfma_f32_16x16x32_bf16 v[76:79], v[252:255], v[184:187], v[76:79]
	v_pk_max_i16 v17, v17, 0
	v_mfma_f32_16x16x32_bf16 v[72:75], v[252:255], v[188:191], v[72:75]
	v_pk_max_i16 v18, v18, 0
	v_mfma_f32_16x16x32_bf16 v[84:87], v[248:251], v[188:191], v[84:87]
	v_pk_max_i16 v19, v19, 0
	ds_read_b128 v[248:251], v121 offset:38912
	ds_read_b128 v[252:255], v121 offset:39936
	s_setprio 0
	s_waitcnt lgkmcnt(6)
	v_mfma_f32_16x16x32_bf16 v[80:83], v[224:227], v[192:195], v[80:83]
	v_pk_max_i16 v20, v20, 0
	v_mfma_f32_16x16x32_bf16 v[76:79], v[228:231], v[192:195], v[76:79]
	v_pk_max_i16 v21, v21, 0
	v_mfma_f32_16x16x32_bf16 v[72:75], v[228:231], v[196:199], v[72:75]
	v_pk_max_i16 v22, v22, 0
	v_mfma_f32_16x16x32_bf16 v[84:87], v[224:227], v[196:199], v[84:87]
	v_pk_max_i16 v23, v23, 0
	s_waitcnt lgkmcnt(4)
	v_mfma_f32_16x16x32_bf16 v[80:83], v[232:235], v[200:203], v[80:83]
	v_mfma_f32_16x16x32_bf16 v[76:79], v[236:239], v[200:203], v[76:79]
	v_mfma_f32_16x16x32_bf16 v[72:75], v[236:239], v[204:207], v[72:75]
	v_mfma_f32_16x16x32_bf16 v[84:87], v[232:235], v[204:207], v[84:87]
.Lnerf_hid_b6:
	s_waitcnt vmcnt(0) lgkmcnt(0)
	s_barrier
	ds_read_b128 v[224:227], v121 offset:40960
	ds_read_b128 v[228:231], v121 offset:41984
	ds_read_b128 v[64:67], v183 offset:1536
	ds_read_b128 v[56:59], v183 offset:1536
	ds_read_b128 v[68:71], v183 offset:1600
	ds_read_b128 v[60:63], v183 offset:1600
	v_mfma_f32_16x16x32_bf16 v[80:83], v[240:243], v[208:211], v[80:83]
	ds_read_b128 v[232:235], v121 offset:43008
	v_mfma_f32_16x16x32_bf16 v[76:79], v[244:247], v[208:211], v[76:79]
	ds_read_b128 v[236:239], v121 offset:44032
	v_mfma_f32_16x16x32_bf16 v[72:75], v[244:247], v[212:215], v[72:75]
	v_mfma_f32_16x16x32_bf16 v[84:87], v[240:243], v[212:215], v[84:87]
	ds_read_b128 v[240:243], v121 offset:45056
	ds_read_b128 v[244:247], v121 offset:46080
	v_mfma_f32_16x16x32_bf16 v[80:83], v[248:251], v[216:219], v[80:83]
	v_mfma_f32_16x16x32_bf16 v[76:79], v[252:255], v[216:219], v[76:79]
	v_mfma_f32_16x16x32_bf16 v[72:75], v[252:255], v[220:223], v[72:75]
	v_mfma_f32_16x16x32_bf16 v[84:87], v[248:251], v[220:223], v[84:87]
	ds_read_b128 v[248:251], v121 offset:47104
	ds_read_b128 v[252:255], v121 offset:48128
	s_setprio 3
	s_waitcnt lgkmcnt(6)
	v_mfma_f32_16x16x32_bf16 v[64:67], v[224:227], v[88:91], v[64:67]
	v_mfma_f32_16x16x32_bf16 v[68:71], v[228:231], v[88:91], v[68:71]
	v_mfma_f32_16x16x32_bf16 v[60:63], v[228:231], v[92:95], v[60:63]
	v_mfma_f32_16x16x32_bf16 v[56:59], v[224:227], v[92:95], v[56:59]
	ds_read_b128 v[224:227], v121 offset:49152
	ds_read_b128 v[228:231], v121 offset:50176
	s_waitcnt lgkmcnt(6)
	v_mfma_f32_16x16x32_bf16 v[64:67], v[232:235], v[96:99], v[64:67]
	v_cvt_pk_bf16_f32 v24, v80, v81
	v_mfma_f32_16x16x32_bf16 v[68:71], v[236:239], v[96:99], v[68:71]
	s_mov_b32 m0, s35
	s_add_i32 s51, s50, 0x30000
	v_cvt_pk_bf16_f32 v25, v82, v83
	v_mfma_f32_16x16x32_bf16 v[60:63], v[236:239], v[100:103], v[60:63]
	buffer_load_dwordx4 v125, s[36:39], s51 offen lds
	v_cvt_pk_bf16_f32 v26, v76, v77
	v_mfma_f32_16x16x32_bf16 v[56:59], v[232:235], v[100:103], v[56:59]
	v_cvt_pk_bf16_f32 v27, v78, v79
	ds_read_b128 v[232:235], v121 offset:51200
	ds_read_b128 v[236:239], v121 offset:52224
	s_waitcnt lgkmcnt(6)
	v_mfma_f32_16x16x32_bf16 v[64:67], v[240:243], v[104:107], v[64:67]
	v_cvt_pk_bf16_f32 v28, v84, v85
	v_mfma_f32_16x16x32_bf16 v[68:71], v[244:247], v[104:107], v[68:71]
	s_mov_b32 m0, s42
	s_add_i32 s51, s50, 0x32000
	v_cvt_pk_bf16_f32 v29, v86, v87
	v_mfma_f32_16x16x32_bf16 v[60:63], v[244:247], v[108:111], v[60:63]
	buffer_load_dwordx4 v125, s[36:39], s51 offen lds
	v_cvt_pk_bf16_f32 v30, v72, v73
	v_mfma_f32_16x16x32_bf16 v[56:59], v[240:243], v[108:111], v[56:59]
	v_cvt_pk_bf16_f32 v31, v74, v75
	ds_read_b128 v[240:243], v121 offset:53248
	ds_read_b128 v[244:247], v121 offset:54272
	s_waitcnt lgkmcnt(6)
	v_mfma_f32_16x16x32_bf16 v[64:67], v[248:251], v[184:187], v[64:67]
	v_pk_max_i16 v24, v24, 0
	v_mfma_f32_16x16x32_bf16 v[68:71], v[252:255], v[184:187], v[68:71]
	s_mov_b32 m0, s41
	s_add_i32 s51, s50, 0x34000
	v_pk_max_i16 v25, v25, 0
	v_mfma_f32_16x16x32_bf16 v[60:63], v[252:255], v[188:191], v[60:63]
	buffer_load_dwordx4 v125, s[36:39], s51 offen lds
	v_pk_max_i16 v26, v26, 0
	v_mfma_f32_16x16x32_bf16 v[56:59], v[248:251], v[188:191], v[56:59]
	v_pk_max_i16 v27, v27, 0
	ds_read_b128 v[248:251], v121 offset:55296
	ds_read_b128 v[252:255], v121 offset:56320
	s_setprio 2
	s_waitcnt lgkmcnt(6)
	v_mfma_f32_16x16x32_bf16 v[64:67], v[224:227], v[192:195], v[64:67]
	v_pk_max_i16 v28, v28, 0
	v_mfma_f32_16x16x32_bf16 v[68:71], v[228:231], v[192:195], v[68:71]
	s_mov_b32 m0, s40
	s_add_i32 s51, s50, 0x36000
	v_pk_max_i16 v29, v29, 0
	v_mfma_f32_16x16x32_bf16 v[60:63], v[228:231], v[196:199], v[60:63]
	buffer_load_dwordx4 v125, s[36:39], s51 offen lds
	v_pk_max_i16 v30, v30, 0
	v_mfma_f32_16x16x32_bf16 v[56:59], v[224:227], v[196:199], v[56:59]
	v_pk_max_i16 v31, v31, 0
	ds_read_b128 v[224:227], v121 offset:57344
	ds_read_b128 v[228:231], v121 offset:58368
	s_waitcnt lgkmcnt(6)
	v_mfma_f32_16x16x32_bf16 v[64:67], v[232:235], v[200:203], v[64:67]
	ds_read_b128 v[80:83], v183 offset:1664
	ds_read_b128 v[84:87], v183 offset:1664
	ds_read_b128 v[76:79], v183 offset:1728
	ds_read_b128 v[72:75], v183 offset:1728
	v_mfma_f32_16x16x32_bf16 v[68:71], v[236:239], v[200:203], v[68:71]
	v_mfma_f32_16x16x32_bf16 v[60:63], v[236:239], v[204:207], v[60:63]
	v_mfma_f32_16x16x32_bf16 v[56:59], v[232:235], v[204:207], v[56:59]
	ds_read_b128 v[232:235], v121 offset:59392
	ds_read_b128 v[236:239], v121 offset:60416
	s_waitcnt lgkmcnt(10)
	v_mfma_f32_16x16x32_bf16 v[64:67], v[240:243], v[208:211], v[64:67]
	v_mfma_f32_16x16x32_bf16 v[68:71], v[244:247], v[208:211], v[68:71]
	v_mfma_f32_16x16x32_bf16 v[60:63], v[244:247], v[212:215], v[60:63]
	v_mfma_f32_16x16x32_bf16 v[56:59], v[240:243], v[212:215], v[56:59]
	ds_read_b128 v[240:243], v121 offset:61440
	ds_read_b128 v[244:247], v121 offset:62464
	s_waitcnt lgkmcnt(10)
	v_mfma_f32_16x16x32_bf16 v[64:67], v[248:251], v[216:219], v[64:67]
	v_mfma_f32_16x16x32_bf16 v[68:71], v[252:255], v[216:219], v[68:71]
	v_mfma_f32_16x16x32_bf16 v[60:63], v[252:255], v[220:223], v[60:63]
	v_mfma_f32_16x16x32_bf16 v[56:59], v[248:251], v[220:223], v[56:59]
	ds_read_b128 v[248:251], v121 offset:63488
	ds_read_b128 v[252:255], v121 offset:64512
	s_setprio 1
	s_waitcnt lgkmcnt(6)
	v_mfma_f32_16x16x32_bf16 v[80:83], v[224:227], v[88:91], v[80:83]
	v_mfma_f32_16x16x32_bf16 v[76:79], v[228:231], v[88:91], v[76:79]
	v_mfma_f32_16x16x32_bf16 v[72:75], v[228:231], v[92:95], v[72:75]
	v_mfma_f32_16x16x32_bf16 v[84:87], v[224:227], v[92:95], v[84:87]
	ds_read_b128 v[224:227], v126 offset:57344
	ds_read_b128 v[228:231], v126 offset:58368
	s_waitcnt lgkmcnt(6)
	v_mfma_f32_16x16x32_bf16 v[80:83], v[232:235], v[96:99], v[80:83]
	v_cvt_pk_bf16_f32 v32, v64, v65
	v_mfma_f32_16x16x32_bf16 v[76:79], v[236:239], v[96:99], v[76:79]
	v_cvt_pk_bf16_f32 v33, v66, v67
	v_mfma_f32_16x16x32_bf16 v[72:75], v[236:239], v[100:103], v[72:75]
	v_cvt_pk_bf16_f32 v34, v68, v69
	v_mfma_f32_16x16x32_bf16 v[84:87], v[232:235], v[100:103], v[84:87]
	v_cvt_pk_bf16_f32 v35, v70, v71
	ds_read_b128 v[232:235], v126 offset:59392
	ds_read_b128 v[236:239], v126 offset:60416
	s_waitcnt lgkmcnt(6)
	v_mfma_f32_16x16x32_bf16 v[80:83], v[240:243], v[104:107], v[80:83]
	v_cvt_pk_bf16_f32 v36, v56, v57
	v_mfma_f32_16x16x32_bf16 v[76:79], v[244:247], v[104:107], v[76:79]
	v_cvt_pk_bf16_f32 v37, v58, v59
	v_mfma_f32_16x16x32_bf16 v[72:75], v[244:247], v[108:111], v[72:75]
	v_cvt_pk_bf16_f32 v38, v60, v61
	v_mfma_f32_16x16x32_bf16 v[84:87], v[240:243], v[108:111], v[84:87]
	v_cvt_pk_bf16_f32 v39, v62, v63
	ds_read_b128 v[240:243], v126 offset:61440
	ds_read_b128 v[244:247], v126 offset:62464
	s_waitcnt lgkmcnt(6)
	v_mfma_f32_16x16x32_bf16 v[80:83], v[248:251], v[184:187], v[80:83]
	v_pk_max_i16 v32, v32, 0
	v_mfma_f32_16x16x32_bf16 v[76:79], v[252:255], v[184:187], v[76:79]
	v_pk_max_i16 v33, v33, 0
	v_mfma_f32_16x16x32_bf16 v[72:75], v[252:255], v[188:191], v[72:75]
	v_pk_max_i16 v34, v34, 0
	v_mfma_f32_16x16x32_bf16 v[84:87], v[248:251], v[188:191], v[84:87]
	v_pk_max_i16 v35, v35, 0
	ds_read_b128 v[248:251], v126 offset:63488
	ds_read_b128 v[252:255], v126 offset:64512
	s_setprio 0
	s_waitcnt lgkmcnt(6)
	v_mfma_f32_16x16x32_bf16 v[80:83], v[224:227], v[192:195], v[80:83]
	v_pk_max_i16 v36, v36, 0
	v_mfma_f32_16x16x32_bf16 v[76:79], v[228:231], v[192:195], v[76:79]
	v_pk_max_i16 v37, v37, 0
	v_mfma_f32_16x16x32_bf16 v[72:75], v[228:231], v[196:199], v[72:75]
	v_pk_max_i16 v38, v38, 0
	v_mfma_f32_16x16x32_bf16 v[84:87], v[224:227], v[196:199], v[84:87]
	v_pk_max_i16 v39, v39, 0
	s_waitcnt lgkmcnt(4)
	v_mfma_f32_16x16x32_bf16 v[80:83], v[232:235], v[200:203], v[80:83]
	v_mfma_f32_16x16x32_bf16 v[76:79], v[236:239], v[200:203], v[76:79]
	v_mfma_f32_16x16x32_bf16 v[72:75], v[236:239], v[204:207], v[72:75]
	v_mfma_f32_16x16x32_bf16 v[84:87], v[232:235], v[204:207], v[84:87]
.Lnerf_hid_b7:
	s_waitcnt vmcnt(0) lgkmcnt(0)
	s_barrier
	ds_read_b128 v[224:227], v121 offset:8192
	ds_read_b128 v[228:231], v121 offset:9216
	ds_read_b128 v[64:67], v183 offset:1792
	ds_read_b128 v[56:59], v183 offset:1792
	ds_read_b128 v[68:71], v183 offset:1856
	ds_read_b128 v[60:63], v183 offset:1856
	v_mfma_f32_16x16x32_bf16 v[80:83], v[240:243], v[208:211], v[80:83]
	ds_read_b128 v[232:235], v121 offset:10240
	v_mfma_f32_16x16x32_bf16 v[76:79], v[244:247], v[208:211], v[76:79]
	ds_read_b128 v[236:239], v121 offset:11264
	v_mfma_f32_16x16x32_bf16 v[72:75], v[244:247], v[212:215], v[72:75]
	v_mfma_f32_16x16x32_bf16 v[84:87], v[240:243], v[212:215], v[84:87]
	ds_read_b128 v[240:243], v121 offset:12288
	ds_read_b128 v[244:247], v121 offset:13312
	v_mfma_f32_16x16x32_bf16 v[80:83], v[248:251], v[216:219], v[80:83]
	v_mfma_f32_16x16x32_bf16 v[76:79], v[252:255], v[216:219], v[76:79]
	v_mfma_f32_16x16x32_bf16 v[72:75], v[252:255], v[220:223], v[72:75]
	v_mfma_f32_16x16x32_bf16 v[84:87], v[248:251], v[220:223], v[84:87]
	ds_read_b128 v[248:251], v121 offset:14336
	ds_read_b128 v[252:255], v121 offset:15360
	s_setprio 3
	s_waitcnt lgkmcnt(6)
	v_mfma_f32_16x16x32_bf16 v[64:67], v[224:227], v[88:91], v[64:67]
	v_mfma_f32_16x16x32_bf16 v[68:71], v[228:231], v[88:91], v[68:71]
	v_mfma_f32_16x16x32_bf16 v[60:63], v[228:231], v[92:95], v[60:63]
	v_mfma_f32_16x16x32_bf16 v[56:59], v[224:227], v[92:95], v[56:59]
	ds_read_b128 v[224:227], v121 offset:16384
	ds_read_b128 v[228:231], v121 offset:17408
	s_waitcnt lgkmcnt(6)
	v_mfma_f32_16x16x32_bf16 v[64:67], v[232:235], v[96:99], v[64:67]
	v_cvt_pk_bf16_f32 v40, v80, v81
	v_mfma_f32_16x16x32_bf16 v[68:71], v[236:239], v[96:99], v[68:71]
	s_mov_b32 m0, s28
	s_add_i32 s51, s50, 0x38000
	v_cvt_pk_bf16_f32 v41, v82, v83
	v_mfma_f32_16x16x32_bf16 v[60:63], v[236:239], v[100:103], v[60:63]
	buffer_load_dwordx4 v125, s[36:39], s51 offen lds
	v_cvt_pk_bf16_f32 v42, v76, v77
	v_mfma_f32_16x16x32_bf16 v[56:59], v[232:235], v[100:103], v[56:59]
	v_cvt_pk_bf16_f32 v43, v78, v79
	ds_read_b128 v[232:235], v121 offset:18432
	ds_read_b128 v[236:239], v121 offset:19456
	s_waitcnt lgkmcnt(6)
	v_mfma_f32_16x16x32_bf16 v[64:67], v[240:243], v[104:107], v[64:67]
	v_cvt_pk_bf16_f32 v44, v84, v85
	v_mfma_f32_16x16x32_bf16 v[68:71], v[244:247], v[104:107], v[68:71]
	s_mov_b32 m0, s29
	s_add_i32 s51, s50, 0x3a000
	v_cvt_pk_bf16_f32 v45, v86, v87
	v_mfma_f32_16x16x32_bf16 v[60:63], v[244:247], v[108:111], v[60:63]
	buffer_load_dwordx4 v125, s[36:39], s51 offen lds
	v_cvt_pk_bf16_f32 v46, v72, v73
	v_mfma_f32_16x16x32_bf16 v[56:59], v[240:243], v[108:111], v[56:59]
	v_cvt_pk_bf16_f32 v47, v74, v75
	ds_read_b128 v[240:243], v121 offset:20480
	ds_read_b128 v[244:247], v121 offset:21504
	s_waitcnt lgkmcnt(6)
	v_mfma_f32_16x16x32_bf16 v[64:67], v[248:251], v[184:187], v[64:67]
	v_pk_max_i16 v40, v40, 0
	v_mfma_f32_16x16x32_bf16 v[68:71], v[252:255], v[184:187], v[68:71]
	s_mov_b32 m0, s33
	s_add_i32 s51, s50, 0x3c000
	v_pk_max_i16 v41, v41, 0
	v_mfma_f32_16x16x32_bf16 v[60:63], v[252:255], v[188:191], v[60:63]
	buffer_load_dwordx4 v125, s[36:39], s51 offen lds
	v_pk_max_i16 v42, v42, 0
	v_mfma_f32_16x16x32_bf16 v[56:59], v[248:251], v[188:191], v[56:59]
	v_pk_max_i16 v43, v43, 0
	ds_read_b128 v[248:251], v121 offset:22528
	ds_read_b128 v[252:255], v121 offset:23552
	s_setprio 2
	s_waitcnt lgkmcnt(6)
	v_mfma_f32_16x16x32_bf16 v[64:67], v[224:227], v[192:195], v[64:67]
	v_pk_max_i16 v44, v44, 0
	v_mfma_f32_16x16x32_bf16 v[68:71], v[228:231], v[192:195], v[68:71]
	s_mov_b32 m0, s34
	s_add_i32 s51, s50, 0x3e000
	v_pk_max_i16 v45, v45, 0
	v_mfma_f32_16x16x32_bf16 v[60:63], v[228:231], v[196:199], v[60:63]
	buffer_load_dwordx4 v125, s[36:39], s51 offen lds
	v_pk_max_i16 v46, v46, 0
	v_mfma_f32_16x16x32_bf16 v[56:59], v[224:227], v[196:199], v[56:59]
	v_pk_max_i16 v47, v47, 0
	ds_read_b128 v[224:227], v121 offset:24576
	ds_read_b128 v[228:231], v121 offset:25600
	s_waitcnt lgkmcnt(6)
	v_mfma_f32_16x16x32_bf16 v[64:67], v[232:235], v[200:203], v[64:67]
	ds_read_b128 v[80:83], v183 offset:1920
	ds_read_b128 v[84:87], v183 offset:1920
	ds_read_b128 v[76:79], v183 offset:1984
	ds_read_b128 v[72:75], v183 offset:1984
	v_mfma_f32_16x16x32_bf16 v[68:71], v[236:239], v[200:203], v[68:71]
	v_mfma_f32_16x16x32_bf16 v[60:63], v[236:239], v[204:207], v[60:63]
	v_mfma_f32_16x16x32_bf16 v[56:59], v[232:235], v[204:207], v[56:59]
	ds_read_b128 v[232:235], v121 offset:26624
	ds_read_b128 v[236:239], v121 offset:27648
	s_waitcnt lgkmcnt(10)
	v_mfma_f32_16x16x32_bf16 v[64:67], v[240:243], v[208:211], v[64:67]
	v_mfma_f32_16x16x32_bf16 v[68:71], v[244:247], v[208:211], v[68:71]
	v_mfma_f32_16x16x32_bf16 v[60:63], v[244:247], v[212:215], v[60:63]
	v_mfma_f32_16x16x32_bf16 v[56:59], v[240:243], v[212:215], v[56:59]
	ds_read_b128 v[240:243], v121 offset:28672
	ds_read_b128 v[244:247], v121 offset:29696
	s_waitcnt lgkmcnt(10)
	v_mfma_f32_16x16x32_bf16 v[64:67], v[248:251], v[216:219], v[64:67]
	v_mfma_f32_16x16x32_bf16 v[68:71], v[252:255], v[216:219], v[68:71]
	v_mfma_f32_16x16x32_bf16 v[60:63], v[252:255], v[220:223], v[60:63]
	v_mfma_f32_16x16x32_bf16 v[56:59], v[248:251], v[220:223], v[56:59]
	ds_read_b128 v[248:251], v121 offset:30720
	ds_read_b128 v[252:255], v121 offset:31744
	s_setprio 1
	s_waitcnt lgkmcnt(6)
	v_mfma_f32_16x16x32_bf16 v[80:83], v[224:227], v[88:91], v[80:83]
	v_mfma_f32_16x16x32_bf16 v[76:79], v[228:231], v[88:91], v[76:79]
	v_mfma_f32_16x16x32_bf16 v[72:75], v[228:231], v[92:95], v[72:75]
	v_mfma_f32_16x16x32_bf16 v[84:87], v[224:227], v[92:95], v[84:87]
	ds_read_b128 v[224:227], v121 offset:32768
	ds_read_b128 v[228:231], v121 offset:33792
	s_waitcnt lgkmcnt(6)
	v_mfma_f32_16x16x32_bf16 v[80:83], v[232:235], v[96:99], v[80:83]
	v_cvt_pk_bf16_f32 v48, v64, v65
	v_mfma_f32_16x16x32_bf16 v[76:79], v[236:239], v[96:99], v[76:79]
	v_cvt_pk_bf16_f32 v49, v66, v67
	v_mfma_f32_16x16x32_bf16 v[72:75], v[236:239], v[100:103], v[72:75]
	v_cvt_pk_bf16_f32 v50, v68, v69
	v_mfma_f32_16x16x32_bf16 v[84:87], v[232:235], v[100:103], v[84:87]
	v_cvt_pk_bf16_f32 v51, v70, v71
	ds_read_b128 v[232:235], v121 offset:34816
	ds_read_b128 v[236:239], v121 offset:35840
	s_waitcnt lgkmcnt(6)
	v_mfma_f32_16x16x32_bf16 v[80:83], v[240:243], v[104:107], v[80:83]
	v_cvt_pk_bf16_f32 v52, v56, v57
	v_mfma_f32_16x16x32_bf16 v[76:79], v[244:247], v[104:107], v[76:79]
	v_cvt_pk_bf16_f32 v53, v58, v59
	v_mfma_f32_16x16x32_bf16 v[72:75], v[244:247], v[108:111], v[72:75]
	v_cvt_pk_bf16_f32 v54, v60, v61
	v_mfma_f32_16x16x32_bf16 v[84:87], v[240:243], v[108:111], v[84:87]
	v_cvt_pk_bf16_f32 v55, v62, v63
	ds_read_b128 v[240:243], v121 offset:36864
	ds_read_b128 v[244:247], v121 offset:37888
	s_waitcnt lgkmcnt(6)
	v_mfma_f32_16x16x32_bf16 v[80:83], v[248:251], v[184:187], v[80:83]
	v_pk_max_i16 v48, v48, 0
	v_mfma_f32_16x16x32_bf16 v[76:79], v[252:255], v[184:187], v[76:79]
	v_pk_max_i16 v49, v49, 0
	v_mfma_f32_16x16x32_bf16 v[72:75], v[252:255], v[188:191], v[72:75]
	v_pk_max_i16 v50, v50, 0
	v_mfma_f32_16x16x32_bf16 v[84:87], v[248:251], v[188:191], v[84:87]
	v_pk_max_i16 v51, v51, 0
	ds_read_b128 v[248:251], v121 offset:38912
	ds_read_b128 v[252:255], v121 offset:39936
	s_setprio 0
	s_waitcnt lgkmcnt(6)
	v_mfma_f32_16x16x32_bf16 v[80:83], v[224:227], v[192:195], v[80:83]
	v_pk_max_i16 v52, v52, 0
	v_mfma_f32_16x16x32_bf16 v[76:79], v[228:231], v[192:195], v[76:79]
	v_pk_max_i16 v53, v53, 0
	v_mfma_f32_16x16x32_bf16 v[72:75], v[228:231], v[196:199], v[72:75]
	v_pk_max_i16 v54, v54, 0
	v_mfma_f32_16x16x32_bf16 v[84:87], v[224:227], v[196:199], v[84:87]
	v_pk_max_i16 v55, v55, 0
	s_waitcnt lgkmcnt(4)
	v_mfma_f32_16x16x32_bf16 v[80:83], v[232:235], v[200:203], v[80:83]
	v_mfma_f32_16x16x32_bf16 v[76:79], v[236:239], v[200:203], v[76:79]
	v_mfma_f32_16x16x32_bf16 v[72:75], v[236:239], v[204:207], v[72:75]
	v_mfma_f32_16x16x32_bf16 v[84:87], v[232:235], v[204:207], v[84:87]
	s_add_i32 s50, s50, 0x40000
	v_add_u32_e32 v183, 0x800, v183
	s_add_i32 s52, s52, 1
	s_branch .Lnerf_hid_b0
.Lnerf_head:
	s_waitcnt vmcnt(0) lgkmcnt(0)
	s_barrier
	ds_read_b128 v[224:227], v121 offset:40960
	ds_read_b128 v[228:231], v121 offset:41984
	ds_read_b128 v[4:7], v183 offset:1024
	ds_read_b128 v[0:3], v183 offset:1024
	v_mfma_f32_16x16x32_bf16 v[80:83], v[240:243], v[48:51], v[80:83]
	ds_read_b128 v[232:235], v121 offset:43008
	v_mfma_f32_16x16x32_bf16 v[76:79], v[244:247], v[48:51], v[76:79]
	ds_read_b128 v[236:239], v121 offset:44032
	v_mfma_f32_16x16x32_bf16 v[72:75], v[244:247], v[52:55], v[72:75]
	v_mfma_f32_16x16x32_bf16 v[84:87], v[240:243], v[52:55], v[84:87]
	ds_read_b128 v[240:243], v121 offset:45056
	ds_read_b128 v[244:247], v121 offset:46080
	v_mfma_f32_16x16x32_bf16 v[80:83], v[248:251], v[112:115], v[80:83]
	v_mfma_f32_16x16x32_bf16 v[76:79], v[252:255], v[112:115], v[76:79]
	v_mfma_f32_16x16x32_bf16 v[72:75], v[252:255], v[116:119], v[72:75]
	v_mfma_f32_16x16x32_bf16 v[84:87], v[248:251], v[116:119], v[84:87]
	ds_read_b128 v[248:251], v121 offset:47104
	ds_read_b128 v[252:255], v121 offset:48128
	s_waitcnt lgkmcnt(7)
	v_mfma_f32_16x16x32_bf16 v[4:7], v[224:227], v[88:91], v[4:7]
	s_waitcnt lgkmcnt(6)
	v_mfma_f32_16x16x32_bf16 v[0:3], v[224:227], v[92:95], v[0:3]
	v_cvt_pk_bf16_f32 v216, v80, v81
	v_cvt_pk_bf16_f32 v217, v82, v83
	v_mfma_f32_16x16x32_bf16 v[4:7], v[228:231], v[96:99], v[4:7]
	v_cvt_pk_bf16_f32 v218, v76, v77
	v_cvt_pk_bf16_f32 v219, v78, v79
	v_mfma_f32_16x16x32_bf16 v[0:3], v[228:231], v[100:103], v[0:3]
	v_cvt_pk_bf16_f32 v220, v84, v85
	v_cvt_pk_bf16_f32 v221, v86, v87
	s_waitcnt lgkmcnt(5)
	v_mfma_f32_16x16x32_bf16 v[4:7], v[232:235], v[104:107], v[4:7]
	v_cvt_pk_bf16_f32 v222, v72, v73
	v_cvt_pk_bf16_f32 v223, v74, v75
	v_mfma_f32_16x16x32_bf16 v[0:3], v[232:235], v[108:111], v[0:3]
	v_pk_max_i16 v216, v216, 0
	v_pk_max_i16 v217, v217, 0
	s_waitcnt lgkmcnt(4)
	v_mfma_f32_16x16x32_bf16 v[4:7], v[236:239], v[184:187], v[4:7]
	v_pk_max_i16 v218, v218, 0
	v_pk_max_i16 v219, v219, 0
	v_mfma_f32_16x16x32_bf16 v[0:3], v[236:239], v[188:191], v[0:3]
	v_pk_max_i16 v220, v220, 0
	v_pk_max_i16 v221, v221, 0
	s_waitcnt lgkmcnt(3)
	v_mfma_f32_16x16x32_bf16 v[4:7], v[240:243], v[192:195], v[4:7]
	v_pk_max_i16 v222, v222, 0
	v_pk_max_i16 v223, v223, 0
	v_mfma_f32_16x16x32_bf16 v[0:3], v[240:243], v[196:199], v[0:3]
	s_waitcnt lgkmcnt(2)
	v_mfma_f32_16x16x32_bf16 v[4:7], v[244:247], v[200:203], v[4:7]
	v_mfma_f32_16x16x32_bf16 v[0:3], v[244:247], v[204:207], v[0:3]
	s_waitcnt lgkmcnt(1)
	v_mfma_f32_16x16x32_bf16 v[4:7], v[248:251], v[208:211], v[4:7]
	v_mfma_f32_16x16x32_bf16 v[0:3], v[248:251], v[212:215], v[0:3]
	s_nop 1
	s_waitcnt lgkmcnt(0)
	v_mfma_f32_16x16x32_bf16 v[4:7], v[252:255], v[216:219], v[4:7]
	v_mfma_f32_16x16x32_bf16 v[0:3], v[252:255], v[220:223], v[0:3]
	s_nop 7
	s_nop 1
	s_setprio 0
	s_and_saveexec_b64 s[20:21], s[2:3]
	s_cbranch_execz .LBB1_20
	s_nop 4
	v_mul_f32_e32 v6, 0xbfb8aa3b, v6
	v_mul_f32_e32 v7, 0xbfb8aa3b, v7
	v_exp_f32_e32 v6, v6
	v_exp_f32_e32 v7, v7
	v_mul_f32_e32 v4, 0xbfb8aa3b, v4
	v_mul_f32_e32 v5, 0xbfb8aa3b, v5
	v_exp_f32_e32 v4, v4
	v_pk_add_f32 v[6:7], v[6:7], 1.0 op_sel_hi:[1,0]
	v_exp_f32_e32 v5, v5
	v_div_scale_f32 v8, s[24:25], v7, v7, 1.0
	v_rcp_f32_e32 v9, v8
	s_lshl_b32 s24, s45, 6
	s_add_i32 s47, s43, s24
	v_pk_add_f32 v[4:5], v[4:5], 1.0 op_sel_hi:[1,0]
	v_fma_f32 v10, -v8, v9, 1.0
	v_fmac_f32_e32 v9, v10, v9
	v_div_scale_f32 v10, vcc, 1.0, v7, 1.0
	v_mul_f32_e32 v11, v10, v9
	v_fma_f32 v12, -v8, v11, v10
	v_fmac_f32_e32 v11, v12, v9
	v_fma_f32 v8, -v8, v11, v10
	v_div_scale_f32 v10, s[24:25], v6, v6, 1.0
	v_rcp_f32_e32 v12, v10
	v_div_fmas_f32 v8, v8, v9, v11
	v_div_fixup_f32 v7, v8, v7, 1.0
	v_fma_f32 v8, -v10, v12, 1.0
	v_fmac_f32_e32 v12, v8, v12
	v_div_scale_f32 v8, vcc, 1.0, v6, 1.0
	v_mul_f32_e32 v9, v8, v12
	v_fma_f32 v11, -v10, v9, v8
	v_fmac_f32_e32 v9, v11, v12
	v_fma_f32 v8, -v10, v9, v8
	v_div_scale_f32 v10, s[24:25], v5, v5, 1.0
	v_rcp_f32_e32 v11, v10
	v_div_fmas_f32 v8, v8, v12, v9
	v_div_fixup_f32 v6, v8, v6, 1.0
	v_fma_f32 v8, -v10, v11, 1.0
	v_fmac_f32_e32 v11, v8, v11
	v_div_scale_f32 v8, vcc, 1.0, v5, 1.0
	v_mul_f32_e32 v9, v8, v11
	v_fma_f32 v12, -v10, v9, v8
	v_fmac_f32_e32 v9, v12, v11
	v_fma_f32 v8, -v10, v9, v8
	v_div_scale_f32 v10, s[24:25], v4, v4, 1.0
	v_rcp_f32_e32 v12, v10
	v_div_fmas_f32 v8, v8, v11, v9
	v_div_fixup_f32 v5, v8, v5, 1.0
	s_mov_b64 s[24:25], -1
	v_fma_f32 v8, -v10, v12, 1.0
	v_fmac_f32_e32 v12, v8, v12
	v_div_scale_f32 v8, vcc, 1.0, v4, 1.0
	v_mul_f32_e32 v9, v8, v12
	v_fma_f32 v11, -v10, v9, v8
	v_fmac_f32_e32 v9, v11, v12
	v_fma_f32 v8, -v10, v9, v8
	v_div_fmas_f32 v8, v8, v12, v9
	v_div_fixup_f32 v4, v8, v4, 1.0
	s_and_b64 vcc, exec, s[16:17]
	s_cbranch_vccz .LBB1_14
	v_or_b32_e32 v8, s47, v130
	v_lshl_add_u32 v8, v8, 4, v182
	ds_write_b128 v8, v[4:7]
	s_mov_b64 s[24:25], 0
